# in-proj store_tile8 epilogue (gelu u/v tiles incl. LayerNorm partial sums, plain v_attn tiles) rewritten by hand: 7 VALU per gelu element with the row factor folded into polynomial coefficients and th
# speedup vs baseline: 1.0171x; 1.0062x over previous
; __device__ __forceinline__ u32x4 pack8(const f32x4 a, const f32x4 b) { u32x4 w; w.x = cvt_pk_bf16(a[0], a[1]); w.y = cvt_pk_bf16(a[2], a[3]); w.z = cvt_pk_bf16(b[0], b[1]); w.w = cvt_pk_bf16(b[2], b[3]); return w; }
;     const float c0 = act == 1 ? -2.302208198f : -1.4426950408889634f, c1 = act == 1 ? -0.10294324f : 0.f;
; #pragma unroll
;     for (int ai = 0; ai < 2; ++ai) { if (ai == 1 && halfunit) break;
; #pragma unroll
;         for (int m = 0; m < 4; ++m) { bf16_t* rowp = base + (size_t)(row0 + ai * HALF + m * 16) * ldc + col0; float ls1 = 0.f, ls2 = 0.f; const float rf = rsr[ai * HALF + m * 16];
; #pragma unroll
;             for (int bj = 0; bj < 2; ++bj) { f32x4 v0 = acc[ai][bj][m][0] * rf, v1 = acc[ai][bj][m][1] * rf;
;                 if (act != 0) {
; #pragma unroll
;                     for (int e = 0; e < 4; ++e) { const float x0 = v0[e], x1 = v1[e];
;                         const float r0 = __builtin_amdgcn_rcpf(1.0f + __builtin_amdgcn_exp2f(x0 * (c0 + c1 * x0 * x0))), r1 = __builtin_amdgcn_rcpf(1.0f + __builtin_amdgcn_exp2f(x1 * (c0 + c1 * x1 * x1)));
;                         v0[e] = act == 1 ? x0 * r0 : r0; v1[e] = act == 1 ? x1 * r1 : r1; } }
;                 if (stat) {
; #pragma unroll
;                     for (int e = 0; e < 4; ++e) { ls1 += v0[e] + v1[e]; ls2 += v0[e] * v0[e] + v1[e] * v1[e]; } }
;                 *(u32x4*)(rowp + bj * HALF) = pack8(v0, v1); }
;             if (stat) { ls1 = xor_add<16>(ls1); ls1 = xor_add<32>(ls1); ls2 = xor_add<16>(ls2); ls2 = xor_add<32>(ls2);
;                 if (fq == 0) { f32x2 st2; st2.x = ls1; st2.y = ls2; *(f32x2*)(stat + (size_t)(row0 + ai * HALF + m * 16) * 16) = st2; } }
;             asm volatile("" ::: "memory"); } }
;     __device__ __forceinline__ void operator()(const f32x4 (&acc)[2][2][4][2], const Unit& u, int wr, int wc, int fr, int fq) const {
;     ...
;             bf16_t* base = (bf16_t*)(wsb + (pn < 2 ? WS_U : (pn < 4 ? WS_VG : WS_VA))); const int ldc = 512, pc = pn < 2 ? pn : (pn < 4 ? pn - 2 : pn - 8), act = pn < 4 ? 1 : 0;
;             float* stat = (pn == 2 || pn == 3) ? (float*)(wsb + WS_STAT) + ((pn - 2) * 4 + wc) * 2 : nullptr;
;             if (pn < 10) store_tile8(acc, rsr, base, ldc, row0, pc * 256 + cl, act, u.half != 0, stat, fq);
.LBB0_401:
	s_andn2_b64 vcc, exec, s[0:1]
	s_cbranch_vccnz .LBB0_537
	ds_read_b32 v156, v205
	s_mov_b32 s0, 0xe000000
	s_cmp_lt_i32 s70, 4
	s_cselect_b32 s0, 0xc000000, s0
	s_cmp_lt_i32 s70, 2
	s_cselect_b32 s0, 0xa000000, s0
	s_and_b32 s1, s70, 1
	s_lshl_b32 s1, s1, 9
	s_add_i32 s0, s0, s1
	s_add_u32 s0, s16, s0
	s_addc_u32 s1, s17, 0
	v_ashrrev_i32_e32 v133, 31, v132
	v_lshlrev_b64 v[134:135], 10, v[132:133]
	v_lshl_add_u64 v[136:137], v[172:173], 1, s[0:1]
	v_lshl_add_u64 v[134:135], v[136:137], 0, v[134:135]
	s_lshl_b32 s8, s70, 3
	s_add_i32 s8, s74, s8
	s_ashr_i32 s9, s8, 31
	s_lshl_b64 s[8:9], s[8:9], 2
	s_add_u32 s38, s75, s8
	s_addc_u32 s39, s76, s9
	v_lshlrev_b64 v[138:139], 6, v[132:133]
	v_lshl_add_u64 v[138:139], v[138:139], 0, s[38:39]
	s_cmp_lt_i32 s70, 2
	s_cbranch_scc1 .Lt8_gelu
	s_cmp_lt_i32 s70, 4
	s_cbranch_scc1 .Lt8_gstat
	s_waitcnt lgkmcnt(0)
	ds_read_b32 v160, v205 offset:64
	v_mul_f32_e32 v128, v156, v128
	v_mul_f32_e32 v129, v156, v129
	v_mul_f32_e32 v130, v156, v130
	v_mul_f32_e32 v131, v156, v131
	v_mul_f32_e32 v124, v156, v124
	v_mul_f32_e32 v125, v156, v125
	v_mul_f32_e32 v126, v156, v126
	v_mul_f32_e32 v127, v156, v127
	v_mul_f32_e32 v120, v156, v120
	v_mul_f32_e32 v121, v156, v121
	v_mul_f32_e32 v122, v156, v122
	v_mul_f32_e32 v123, v156, v123
	v_mul_f32_e32 v116, v156, v116
	v_mul_f32_e32 v117, v156, v117
	v_mul_f32_e32 v118, v156, v118
	v_mul_f32_e32 v119, v156, v119
	v_cvt_pk_bf16_f32 v128, v128, v129
	v_cvt_pk_bf16_f32 v129, v130, v131
	v_cvt_pk_bf16_f32 v130, v124, v125
	v_cvt_pk_bf16_f32 v131, v126, v127
	global_store_dwordx4 v[134:135], v[128:131], off
	v_cvt_pk_bf16_f32 v120, v120, v121
	v_cvt_pk_bf16_f32 v121, v122, v123
	v_cvt_pk_bf16_f32 v122, v116, v117
	v_cvt_pk_bf16_f32 v123, v118, v119
	global_store_dwordx4 v[134:135], v[120:123], off offset:256
	s_waitcnt lgkmcnt(0)
	v_mov_b32_e32 v156, v160
	ds_read_b32 v160, v205 offset:128
	v_mul_f32_e32 v112, v156, v112
	v_mul_f32_e32 v113, v156, v113
	v_mul_f32_e32 v114, v156, v114
	v_mul_f32_e32 v115, v156, v115
	v_mul_f32_e32 v108, v156, v108
	v_mul_f32_e32 v109, v156, v109
	v_mul_f32_e32 v110, v156, v110
	v_mul_f32_e32 v111, v156, v111
	v_mul_f32_e32 v104, v156, v104
	v_mul_f32_e32 v105, v156, v105
	v_mul_f32_e32 v106, v156, v106
	v_mul_f32_e32 v107, v156, v107
	v_mul_f32_e32 v100, v156, v100
	v_mul_f32_e32 v101, v156, v101
	v_mul_f32_e32 v102, v156, v102
	v_mul_f32_e32 v103, v156, v103
	s_mov_b64 s[0:1], 0x4000
	v_lshl_add_u64 v[136:137], v[134:135], 0, s[0:1]
	v_cvt_pk_bf16_f32 v112, v112, v113
	v_cvt_pk_bf16_f32 v113, v114, v115
	v_cvt_pk_bf16_f32 v114, v108, v109
	v_cvt_pk_bf16_f32 v115, v110, v111
	global_store_dwordx4 v[136:137], v[112:115], off
	v_cvt_pk_bf16_f32 v104, v104, v105
	v_cvt_pk_bf16_f32 v105, v106, v107
	v_cvt_pk_bf16_f32 v106, v100, v101
	v_cvt_pk_bf16_f32 v107, v102, v103
	global_store_dwordx4 v[136:137], v[104:107], off offset:256
	s_waitcnt lgkmcnt(0)
	v_mov_b32_e32 v156, v160
	ds_read_b32 v160, v205 offset:192
	v_mul_f32_e32 v96, v156, v96
	v_mul_f32_e32 v97, v156, v97
	v_mul_f32_e32 v98, v156, v98
	v_mul_f32_e32 v99, v156, v99
	v_mul_f32_e32 v92, v156, v92
	v_mul_f32_e32 v93, v156, v93
	v_mul_f32_e32 v94, v156, v94
	v_mul_f32_e32 v95, v156, v95
	v_mul_f32_e32 v88, v156, v88
	v_mul_f32_e32 v89, v156, v89
	v_mul_f32_e32 v90, v156, v90
	v_mul_f32_e32 v91, v156, v91
	v_mul_f32_e32 v84, v156, v84
	v_mul_f32_e32 v85, v156, v85
	v_mul_f32_e32 v86, v156, v86
	v_mul_f32_e32 v87, v156, v87
	s_mov_b64 s[0:1], 0x8000
	v_lshl_add_u64 v[136:137], v[134:135], 0, s[0:1]
	v_cvt_pk_bf16_f32 v96, v96, v97
	v_cvt_pk_bf16_f32 v97, v98, v99
	v_cvt_pk_bf16_f32 v98, v92, v93
	v_cvt_pk_bf16_f32 v99, v94, v95
	global_store_dwordx4 v[136:137], v[96:99], off
	v_cvt_pk_bf16_f32 v88, v88, v89
	v_cvt_pk_bf16_f32 v89, v90, v91
	v_cvt_pk_bf16_f32 v90, v84, v85
	v_cvt_pk_bf16_f32 v91, v86, v87
	global_store_dwordx4 v[136:137], v[88:91], off offset:256
	s_waitcnt lgkmcnt(0)
	v_mov_b32_e32 v156, v160
	ds_read_b32 v160, v205 offset:512
	v_mul_f32_e32 v80, v156, v80
	v_mul_f32_e32 v81, v156, v81
	v_mul_f32_e32 v82, v156, v82
	v_mul_f32_e32 v83, v156, v83
	v_mul_f32_e32 v76, v156, v76
	v_mul_f32_e32 v77, v156, v77
	v_mul_f32_e32 v78, v156, v78
	v_mul_f32_e32 v79, v156, v79
	v_mul_f32_e32 v72, v156, v72
	v_mul_f32_e32 v73, v156, v73
	v_mul_f32_e32 v74, v156, v74
	v_mul_f32_e32 v75, v156, v75
	v_mul_f32_e32 v68, v156, v68
	v_mul_f32_e32 v69, v156, v69
	v_mul_f32_e32 v70, v156, v70
	v_mul_f32_e32 v71, v156, v71
	s_mov_b64 s[0:1], 0xc000
	v_lshl_add_u64 v[136:137], v[134:135], 0, s[0:1]
	v_cvt_pk_bf16_f32 v80, v80, v81
	v_cvt_pk_bf16_f32 v81, v82, v83
	v_cvt_pk_bf16_f32 v82, v76, v77
	v_cvt_pk_bf16_f32 v83, v78, v79
	global_store_dwordx4 v[136:137], v[80:83], off
	v_cvt_pk_bf16_f32 v72, v72, v73
	v_cvt_pk_bf16_f32 v73, v74, v75
	v_cvt_pk_bf16_f32 v74, v68, v69
	v_cvt_pk_bf16_f32 v75, v70, v71
	global_store_dwordx4 v[136:137], v[72:75], off offset:256
	s_waitcnt lgkmcnt(0)
	v_mov_b32_e32 v156, v160
	ds_read_b32 v160, v205 offset:576
	v_mul_f32_e32 v64, v156, v64
	v_mul_f32_e32 v65, v156, v65
	v_mul_f32_e32 v66, v156, v66
	v_mul_f32_e32 v67, v156, v67
	v_mul_f32_e32 v60, v156, v60
	v_mul_f32_e32 v61, v156, v61
	v_mul_f32_e32 v62, v156, v62
	v_mul_f32_e32 v63, v156, v63
	v_mul_f32_e32 v56, v156, v56
	v_mul_f32_e32 v57, v156, v57
	v_mul_f32_e32 v58, v156, v58
	v_mul_f32_e32 v59, v156, v59
	v_mul_f32_e32 v52, v156, v52
	v_mul_f32_e32 v53, v156, v53
	v_mul_f32_e32 v54, v156, v54
	v_mul_f32_e32 v55, v156, v55
	s_mov_b64 s[0:1], 0x20000
	v_lshl_add_u64 v[136:137], v[134:135], 0, s[0:1]
	v_cvt_pk_bf16_f32 v64, v64, v65
	v_cvt_pk_bf16_f32 v65, v66, v67
	v_cvt_pk_bf16_f32 v66, v60, v61
	v_cvt_pk_bf16_f32 v67, v62, v63
	global_store_dwordx4 v[136:137], v[64:67], off
	v_cvt_pk_bf16_f32 v56, v56, v57
	v_cvt_pk_bf16_f32 v57, v58, v59
	v_cvt_pk_bf16_f32 v58, v52, v53
	v_cvt_pk_bf16_f32 v59, v54, v55
	global_store_dwordx4 v[136:137], v[56:59], off offset:256
	s_waitcnt lgkmcnt(0)
; __device__ __forceinline__ u32x4 pack8(const f32x4 a, const f32x4 b) { u32x4 w; w.x = cvt_pk_bf16(a[0], a[1]); w.y = cvt_pk_bf16(a[2], a[3]); w.z = cvt_pk_bf16(b[0], b[1]); w.w = cvt_pk_bf16(b[2], b[3]); return w; }
;     const float c0 = act == 1 ? -2.302208198f : -1.4426950408889634f, c1 = act == 1 ? -0.10294324f : 0.f;
; #pragma unroll
;     for (int ai = 0; ai < 2; ++ai) { if (ai == 1 && halfunit) break;
; #pragma unroll
;         for (int m = 0; m < 4; ++m) { bf16_t* rowp = base + (size_t)(row0 + ai * HALF + m * 16) * ldc + col0; float ls1 = 0.f, ls2 = 0.f; const float rf = rsr[ai * HALF + m * 16];
; #pragma unroll
;             for (int bj = 0; bj < 2; ++bj) { f32x4 v0 = acc[ai][bj][m][0] * rf, v1 = acc[ai][bj][m][1] * rf;
;                 if (act != 0) {
; #pragma unroll
;                     for (int e = 0; e < 4; ++e) { const float x0 = v0[e], x1 = v1[e];
;                         const float r0 = __builtin_amdgcn_rcpf(1.0f + __builtin_amdgcn_exp2f(x0 * (c0 + c1 * x0 * x0))), r1 = __builtin_amdgcn_rcpf(1.0f + __builtin_amdgcn_exp2f(x1 * (c0 + c1 * x1 * x1)));
;                         v0[e] = act == 1 ? x0 * r0 : r0; v1[e] = act == 1 ? x1 * r1 : r1; } }
;                 if (stat) {
; #pragma unroll
;                     for (int e = 0; e < 4; ++e) { ls1 += v0[e] + v1[e]; ls2 += v0[e] * v0[e] + v1[e] * v1[e]; } }
;                 *(u32x4*)(rowp + bj * HALF) = pack8(v0, v1); }
;             if (stat) { ls1 = xor_add<16>(ls1); ls1 = xor_add<32>(ls1); ls2 = xor_add<16>(ls2); ls2 = xor_add<32>(ls2);
;                 if (fq == 0) { f32x2 st2; st2.x = ls1; st2.y = ls2; *(f32x2*)(stat + (size_t)(row0 + ai * HALF + m * 16) * 16) = st2; } }
;             asm volatile("" ::: "memory"); } }
; }
	v_mov_b32_e32 v156, v160
	ds_read_b32 v160, v205 offset:640
	v_mul_f32_e32 v48, v156, v48
	v_mul_f32_e32 v49, v156, v49
	v_mul_f32_e32 v50, v156, v50
	v_mul_f32_e32 v51, v156, v51
	v_mul_f32_e32 v44, v156, v44
	v_mul_f32_e32 v45, v156, v45
	v_mul_f32_e32 v46, v156, v46
	v_mul_f32_e32 v47, v156, v47
	v_mul_f32_e32 v40, v156, v40
	v_mul_f32_e32 v41, v156, v41
	v_mul_f32_e32 v42, v156, v42
	v_mul_f32_e32 v43, v156, v43
	v_mul_f32_e32 v36, v156, v36
	v_mul_f32_e32 v37, v156, v37
	v_mul_f32_e32 v38, v156, v38
	v_mul_f32_e32 v39, v156, v39
	s_mov_b64 s[0:1], 0x24000
	v_lshl_add_u64 v[136:137], v[134:135], 0, s[0:1]
	v_cvt_pk_bf16_f32 v48, v48, v49
	v_cvt_pk_bf16_f32 v49, v50, v51
	v_cvt_pk_bf16_f32 v50, v44, v45
	v_cvt_pk_bf16_f32 v51, v46, v47
	global_store_dwordx4 v[136:137], v[48:51], off
	v_cvt_pk_bf16_f32 v40, v40, v41
	v_cvt_pk_bf16_f32 v41, v42, v43
	v_cvt_pk_bf16_f32 v42, v36, v37
	v_cvt_pk_bf16_f32 v43, v38, v39
	global_store_dwordx4 v[136:137], v[40:43], off offset:256
	s_waitcnt lgkmcnt(0)
	v_mov_b32_e32 v156, v160
	ds_read_b32 v160, v205 offset:704
	v_mul_f32_e32 v32, v156, v32
	v_mul_f32_e32 v33, v156, v33
	v_mul_f32_e32 v34, v156, v34
	v_mul_f32_e32 v35, v156, v35
	v_mul_f32_e32 v28, v156, v28
	v_mul_f32_e32 v29, v156, v29
	v_mul_f32_e32 v30, v156, v30
	v_mul_f32_e32 v31, v156, v31
	v_mul_f32_e32 v24, v156, v24
	v_mul_f32_e32 v25, v156, v25
	v_mul_f32_e32 v26, v156, v26
	v_mul_f32_e32 v27, v156, v27
	v_mul_f32_e32 v20, v156, v20
	v_mul_f32_e32 v21, v156, v21
	v_mul_f32_e32 v22, v156, v22
	v_mul_f32_e32 v23, v156, v23
	s_mov_b64 s[0:1], 0x28000
	v_lshl_add_u64 v[136:137], v[134:135], 0, s[0:1]
	v_cvt_pk_bf16_f32 v32, v32, v33
	v_cvt_pk_bf16_f32 v33, v34, v35
	v_cvt_pk_bf16_f32 v34, v28, v29
	v_cvt_pk_bf16_f32 v35, v30, v31
	global_store_dwordx4 v[136:137], v[32:35], off
	v_cvt_pk_bf16_f32 v24, v24, v25
	v_cvt_pk_bf16_f32 v25, v26, v27
	v_cvt_pk_bf16_f32 v26, v20, v21
	v_cvt_pk_bf16_f32 v27, v22, v23
	global_store_dwordx4 v[136:137], v[24:27], off offset:256
	s_waitcnt lgkmcnt(0)
	v_mov_b32_e32 v156, v160
	v_mul_f32_e32 v16, v156, v16
	v_mul_f32_e32 v17, v156, v17
	v_mul_f32_e32 v18, v156, v18
	v_mul_f32_e32 v19, v156, v19
	v_mul_f32_e32 v12, v156, v12
	v_mul_f32_e32 v13, v156, v13
	v_mul_f32_e32 v14, v156, v14
	v_mul_f32_e32 v15, v156, v15
	v_mul_f32_e32 v8, v156, v8
	v_mul_f32_e32 v9, v156, v9
	v_mul_f32_e32 v10, v156, v10
	v_mul_f32_e32 v11, v156, v11
	v_mul_f32_e32 v4, v156, v4
	v_mul_f32_e32 v5, v156, v5
	v_mul_f32_e32 v6, v156, v6
	v_mul_f32_e32 v7, v156, v7
	s_mov_b64 s[0:1], 0x2c000
	v_lshl_add_u64 v[136:137], v[134:135], 0, s[0:1]
	v_cvt_pk_bf16_f32 v16, v16, v17
	v_cvt_pk_bf16_f32 v17, v18, v19
	v_cvt_pk_bf16_f32 v18, v12, v13
	v_cvt_pk_bf16_f32 v19, v14, v15
	global_store_dwordx4 v[136:137], v[16:19], off
	v_cvt_pk_bf16_f32 v8, v8, v9
	v_cvt_pk_bf16_f32 v9, v10, v11
	v_cvt_pk_bf16_f32 v10, v4, v5
	v_cvt_pk_bf16_f32 v11, v6, v7
	global_store_dwordx4 v[136:137], v[8:11], off offset:256
	s_branch .Lt8_end
.Lt8_gelu:
	s_waitcnt lgkmcnt(0)
	ds_read_b32 v160, v205 offset:64
	v_mul_f32_e32 v158, v156, v156
	v_mul_f32_e32 v157, 0xc0135761, v156
	v_rcp_f32_e32 v159, v156
	v_mul_f32_e32 v158, v158, v156
	v_mul_f32_e32 v158, 0xbdd2d3e8, v158
	v_mul_f32_e32 v140, v128, v128
	v_mul_f32_e32 v141, v129, v129
	v_mul_f32_e32 v142, v130, v130
	v_mul_f32_e32 v143, v131, v131
	v_mul_f32_e32 v144, v124, v124
	v_mul_f32_e32 v145, v125, v125
	v_mul_f32_e32 v146, v126, v126
	v_mul_f32_e32 v147, v127, v127
	v_mul_f32_e32 v148, v120, v120
	v_mul_f32_e32 v149, v121, v121
	v_mul_f32_e32 v150, v122, v122
	v_mul_f32_e32 v151, v123, v123
	v_mul_f32_e32 v152, v116, v116
	v_mul_f32_e32 v153, v117, v117
	v_mul_f32_e32 v154, v118, v118
	v_mul_f32_e32 v155, v119, v119
	v_fma_f32 v140, v140, v158, v157
	v_fma_f32 v141, v141, v158, v157
	v_fma_f32 v142, v142, v158, v157
	v_fma_f32 v143, v143, v158, v157
	v_fma_f32 v144, v144, v158, v157
	v_fma_f32 v145, v145, v158, v157
	v_fma_f32 v146, v146, v158, v157
	v_fma_f32 v147, v147, v158, v157
	v_fma_f32 v148, v148, v158, v157
	v_fma_f32 v149, v149, v158, v157
	v_fma_f32 v150, v150, v158, v157
	v_fma_f32 v151, v151, v158, v157
	v_fma_f32 v152, v152, v158, v157
	v_fma_f32 v153, v153, v158, v157
	v_fma_f32 v154, v154, v158, v157
	v_fma_f32 v155, v155, v158, v157
	v_mul_f32_e32 v140, v128, v140
	v_mul_f32_e32 v141, v129, v141
	v_mul_f32_e32 v142, v130, v142
	v_mul_f32_e32 v143, v131, v143
	v_mul_f32_e32 v144, v124, v144
	v_mul_f32_e32 v145, v125, v145
	v_mul_f32_e32 v146, v126, v146
	v_mul_f32_e32 v147, v127, v147
	v_mul_f32_e32 v148, v120, v148
	v_mul_f32_e32 v149, v121, v149
	v_mul_f32_e32 v150, v122, v150
	v_mul_f32_e32 v151, v123, v151
	v_mul_f32_e32 v152, v116, v152
	v_mul_f32_e32 v153, v117, v153
	v_mul_f32_e32 v154, v118, v154
	v_mul_f32_e32 v155, v119, v155
	v_exp_f32_e32 v140, v140
	v_exp_f32_e32 v141, v141
	v_exp_f32_e32 v142, v142
	v_exp_f32_e32 v143, v143
	v_exp_f32_e32 v144, v144
	v_exp_f32_e32 v145, v145
	v_exp_f32_e32 v146, v146
	v_exp_f32_e32 v147, v147
	v_exp_f32_e32 v148, v148
	v_exp_f32_e32 v149, v149
	v_exp_f32_e32 v150, v150
	v_exp_f32_e32 v151, v151
	v_exp_f32_e32 v152, v152
	v_exp_f32_e32 v153, v153
	v_exp_f32_e32 v154, v154
	v_exp_f32_e32 v155, v155
	v_fma_f32 v140, v140, v159, v159
	v_fma_f32 v141, v141, v159, v159
	v_fma_f32 v142, v142, v159, v159
	v_fma_f32 v143, v143, v159, v159
	v_fma_f32 v144, v144, v159, v159
	v_fma_f32 v145, v145, v159, v159
	v_fma_f32 v146, v146, v159, v159
	v_fma_f32 v147, v147, v159, v159
	v_fma_f32 v148, v148, v159, v159
	v_fma_f32 v149, v149, v159, v159
	v_fma_f32 v150, v150, v159, v159
	v_fma_f32 v151, v151, v159, v159
	v_fma_f32 v152, v152, v159, v159
; __device__ __forceinline__ u32x4 pack8(const f32x4 a, const f32x4 b) { u32x4 w; w.x = cvt_pk_bf16(a[0], a[1]); w.y = cvt_pk_bf16(a[2], a[3]); w.z = cvt_pk_bf16(b[0], b[1]); w.w = cvt_pk_bf16(b[2], b[3]); return w; }
;     const float c0 = act == 1 ? -2.302208198f : -1.4426950408889634f, c1 = act == 1 ? -0.10294324f : 0.f;
; #pragma unroll
;     for (int ai = 0; ai < 2; ++ai) { if (ai == 1 && halfunit) break;
; #pragma unroll
;         for (int m = 0; m < 4; ++m) { bf16_t* rowp = base + (size_t)(row0 + ai * HALF + m * 16) * ldc + col0; float ls1 = 0.f, ls2 = 0.f; const float rf = rsr[ai * HALF + m * 16];
; #pragma unroll
;             for (int bj = 0; bj < 2; ++bj) { f32x4 v0 = acc[ai][bj][m][0] * rf, v1 = acc[ai][bj][m][1] * rf;
;                 if (act != 0) {
; #pragma unroll
;                     for (int e = 0; e < 4; ++e) { const float x0 = v0[e], x1 = v1[e];
;                         const float r0 = __builtin_amdgcn_rcpf(1.0f + __builtin_amdgcn_exp2f(x0 * (c0 + c1 * x0 * x0))), r1 = __builtin_amdgcn_rcpf(1.0f + __builtin_amdgcn_exp2f(x1 * (c0 + c1 * x1 * x1)));
;                         v0[e] = act == 1 ? x0 * r0 : r0; v1[e] = act == 1 ? x1 * r1 : r1; } }
;                 if (stat) {
; #pragma unroll
;                     for (int e = 0; e < 4; ++e) { ls1 += v0[e] + v1[e]; ls2 += v0[e] * v0[e] + v1[e] * v1[e]; } }
;                 *(u32x4*)(rowp + bj * HALF) = pack8(v0, v1); }
	v_fma_f32 v153, v153, v159, v159
	v_fma_f32 v154, v154, v159, v159
	v_fma_f32 v155, v155, v159, v159
	v_rcp_f32_e32 v140, v140
	v_rcp_f32_e32 v141, v141
	v_rcp_f32_e32 v142, v142
	v_rcp_f32_e32 v143, v143
	v_rcp_f32_e32 v144, v144
	v_rcp_f32_e32 v145, v145
	v_rcp_f32_e32 v146, v146
	v_rcp_f32_e32 v147, v147
	v_rcp_f32_e32 v148, v148
	v_rcp_f32_e32 v149, v149
	v_rcp_f32_e32 v150, v150
	v_rcp_f32_e32 v151, v151
	v_rcp_f32_e32 v152, v152
	v_rcp_f32_e32 v153, v153
	v_rcp_f32_e32 v154, v154
	v_rcp_f32_e32 v155, v155
	v_mul_f32_e32 v128, v128, v140
	v_mul_f32_e32 v129, v129, v141
	v_mul_f32_e32 v130, v130, v142
	v_mul_f32_e32 v131, v131, v143
	v_mul_f32_e32 v124, v124, v144
	v_mul_f32_e32 v125, v125, v145
	v_mul_f32_e32 v126, v126, v146
	v_mul_f32_e32 v127, v127, v147
	v_mul_f32_e32 v120, v120, v148
	v_mul_f32_e32 v121, v121, v149
	v_mul_f32_e32 v122, v122, v150
	v_mul_f32_e32 v123, v123, v151
	v_mul_f32_e32 v116, v116, v152
	v_mul_f32_e32 v117, v117, v153
	v_mul_f32_e32 v118, v118, v154
	v_mul_f32_e32 v119, v119, v155
	v_cvt_pk_bf16_f32 v128, v128, v129
	v_cvt_pk_bf16_f32 v129, v130, v131
	v_cvt_pk_bf16_f32 v130, v124, v125
	v_cvt_pk_bf16_f32 v131, v126, v127
	global_store_dwordx4 v[134:135], v[128:131], off
	v_cvt_pk_bf16_f32 v120, v120, v121
	v_cvt_pk_bf16_f32 v121, v122, v123
	v_cvt_pk_bf16_f32 v122, v116, v117
	v_cvt_pk_bf16_f32 v123, v118, v119
	global_store_dwordx4 v[134:135], v[120:123], off offset:256
	s_waitcnt lgkmcnt(0)
	v_mov_b32_e32 v156, v160
	ds_read_b32 v160, v205 offset:128
	v_mul_f32_e32 v158, v156, v156
	v_mul_f32_e32 v157, 0xc0135761, v156
	v_rcp_f32_e32 v159, v156
	v_mul_f32_e32 v158, v158, v156
	v_mul_f32_e32 v158, 0xbdd2d3e8, v158
	v_mul_f32_e32 v140, v112, v112
	v_mul_f32_e32 v141, v113, v113
	v_mul_f32_e32 v142, v114, v114
	v_mul_f32_e32 v143, v115, v115
	v_mul_f32_e32 v144, v108, v108
	v_mul_f32_e32 v145, v109, v109
	v_mul_f32_e32 v146, v110, v110
	v_mul_f32_e32 v147, v111, v111
	v_mul_f32_e32 v148, v104, v104
	v_mul_f32_e32 v149, v105, v105
	v_mul_f32_e32 v150, v106, v106
	v_mul_f32_e32 v151, v107, v107
	v_mul_f32_e32 v152, v100, v100
	v_mul_f32_e32 v153, v101, v101
	v_mul_f32_e32 v154, v102, v102
	v_mul_f32_e32 v155, v103, v103
	v_fma_f32 v140, v140, v158, v157
	v_fma_f32 v141, v141, v158, v157
	v_fma_f32 v142, v142, v158, v157
	v_fma_f32 v143, v143, v158, v157
	v_fma_f32 v144, v144, v158, v157
	v_fma_f32 v145, v145, v158, v157
	v_fma_f32 v146, v146, v158, v157
	v_fma_f32 v147, v147, v158, v157
	v_fma_f32 v148, v148, v158, v157
	v_fma_f32 v149, v149, v158, v157
	v_fma_f32 v150, v150, v158, v157
	v_fma_f32 v151, v151, v158, v157
	v_fma_f32 v152, v152, v158, v157
	v_fma_f32 v153, v153, v158, v157
	v_fma_f32 v154, v154, v158, v157
	v_fma_f32 v155, v155, v158, v157
	v_mul_f32_e32 v140, v112, v140
	v_mul_f32_e32 v141, v113, v141
	v_mul_f32_e32 v142, v114, v142
	v_mul_f32_e32 v143, v115, v143
	v_mul_f32_e32 v144, v108, v144
	v_mul_f32_e32 v145, v109, v145
	v_mul_f32_e32 v146, v110, v146
	v_mul_f32_e32 v147, v111, v147
	v_mul_f32_e32 v148, v104, v148
	v_mul_f32_e32 v149, v105, v149
	v_mul_f32_e32 v150, v106, v150
	v_mul_f32_e32 v151, v107, v151
	v_mul_f32_e32 v152, v100, v152
	v_mul_f32_e32 v153, v101, v153
	v_mul_f32_e32 v154, v102, v154
	v_mul_f32_e32 v155, v103, v155
	v_exp_f32_e32 v140, v140
	v_exp_f32_e32 v141, v141
	v_exp_f32_e32 v142, v142
	v_exp_f32_e32 v143, v143
	v_exp_f32_e32 v144, v144
	v_exp_f32_e32 v145, v145
	v_exp_f32_e32 v146, v146
	v_exp_f32_e32 v147, v147
	v_exp_f32_e32 v148, v148
	v_exp_f32_e32 v149, v149
	v_exp_f32_e32 v150, v150
	v_exp_f32_e32 v151, v151
	v_exp_f32_e32 v152, v152
	v_exp_f32_e32 v153, v153
	v_exp_f32_e32 v154, v154
	v_exp_f32_e32 v155, v155
	v_fma_f32 v140, v140, v159, v159
	v_fma_f32 v141, v141, v159, v159
	v_fma_f32 v142, v142, v159, v159
	v_fma_f32 v143, v143, v159, v159
	v_fma_f32 v144, v144, v159, v159
	v_fma_f32 v145, v145, v159, v159
	v_fma_f32 v146, v146, v159, v159
	v_fma_f32 v147, v147, v159, v159
	v_fma_f32 v148, v148, v159, v159
	v_fma_f32 v149, v149, v159, v159
	v_fma_f32 v150, v150, v159, v159
	v_fma_f32 v151, v151, v159, v159
	v_fma_f32 v152, v152, v159, v159
	v_fma_f32 v153, v153, v159, v159
	v_fma_f32 v154, v154, v159, v159
	v_fma_f32 v155, v155, v159, v159
	v_rcp_f32_e32 v140, v140
	v_rcp_f32_e32 v141, v141
	v_rcp_f32_e32 v142, v142
	v_rcp_f32_e32 v143, v143
	v_rcp_f32_e32 v144, v144
	v_rcp_f32_e32 v145, v145
	v_rcp_f32_e32 v146, v146
	v_rcp_f32_e32 v147, v147
	v_rcp_f32_e32 v148, v148
	v_rcp_f32_e32 v149, v149
	v_rcp_f32_e32 v150, v150
	v_rcp_f32_e32 v151, v151
	v_rcp_f32_e32 v152, v152
	v_rcp_f32_e32 v153, v153
	v_rcp_f32_e32 v154, v154
	v_rcp_f32_e32 v155, v155
	v_mul_f32_e32 v112, v112, v140
	v_mul_f32_e32 v113, v113, v141
	v_mul_f32_e32 v114, v114, v142
	v_mul_f32_e32 v115, v115, v143
	v_mul_f32_e32 v108, v108, v144
	v_mul_f32_e32 v109, v109, v145
	v_mul_f32_e32 v110, v110, v146
	v_mul_f32_e32 v111, v111, v147
	v_mul_f32_e32 v104, v104, v148
	v_mul_f32_e32 v105, v105, v149
	v_mul_f32_e32 v106, v106, v150
	v_mul_f32_e32 v107, v107, v151
	v_mul_f32_e32 v100, v100, v152
	v_mul_f32_e32 v101, v101, v153
	v_mul_f32_e32 v102, v102, v154
	v_mul_f32_e32 v103, v103, v155
	s_mov_b64 s[0:1], 0x4000
	v_lshl_add_u64 v[136:137], v[134:135], 0, s[0:1]
	v_cvt_pk_bf16_f32 v112, v112, v113
	v_cvt_pk_bf16_f32 v113, v114, v115
	v_cvt_pk_bf16_f32 v114, v108, v109
	v_cvt_pk_bf16_f32 v115, v110, v111
	global_store_dwordx4 v[136:137], v[112:115], off
	v_cvt_pk_bf16_f32 v104, v104, v105
	v_cvt_pk_bf16_f32 v105, v106, v107
	v_cvt_pk_bf16_f32 v106, v100, v101
	v_cvt_pk_bf16_f32 v107, v102, v103
	global_store_dwordx4 v[136:137], v[104:107], off offset:256
	s_waitcnt lgkmcnt(0)
; __device__ __forceinline__ u32x4 pack8(const f32x4 a, const f32x4 b) { u32x4 w; w.x = cvt_pk_bf16(a[0], a[1]); w.y = cvt_pk_bf16(a[2], a[3]); w.z = cvt_pk_bf16(b[0], b[1]); w.w = cvt_pk_bf16(b[2], b[3]); return w; }
;     const float c0 = act == 1 ? -2.302208198f : -1.4426950408889634f, c1 = act == 1 ? -0.10294324f : 0.f;
; #pragma unroll
;     for (int ai = 0; ai < 2; ++ai) { if (ai == 1 && halfunit) break;
; #pragma unroll
;         for (int m = 0; m < 4; ++m) { bf16_t* rowp = base + (size_t)(row0 + ai * HALF + m * 16) * ldc + col0; float ls1 = 0.f, ls2 = 0.f; const float rf = rsr[ai * HALF + m * 16];
; #pragma unroll
;             for (int bj = 0; bj < 2; ++bj) { f32x4 v0 = acc[ai][bj][m][0] * rf, v1 = acc[ai][bj][m][1] * rf;
;                 if (act != 0) {
; #pragma unroll
;                     for (int e = 0; e < 4; ++e) { const float x0 = v0[e], x1 = v1[e];
;                         const float r0 = __builtin_amdgcn_rcpf(1.0f + __builtin_amdgcn_exp2f(x0 * (c0 + c1 * x0 * x0))), r1 = __builtin_amdgcn_rcpf(1.0f + __builtin_amdgcn_exp2f(x1 * (c0 + c1 * x1 * x1)));
;                         v0[e] = act == 1 ? x0 * r0 : r0; v1[e] = act == 1 ? x1 * r1 : r1; } }
;                 if (stat) {
; #pragma unroll
;                     for (int e = 0; e < 4; ++e) { ls1 += v0[e] + v1[e]; ls2 += v0[e] * v0[e] + v1[e] * v1[e]; } }
;                 *(u32x4*)(rowp + bj * HALF) = pack8(v0, v1); }
	v_mov_b32_e32 v156, v160
	ds_read_b32 v160, v205 offset:192
	v_mul_f32_e32 v158, v156, v156
	v_mul_f32_e32 v157, 0xc0135761, v156
	v_rcp_f32_e32 v159, v156
	v_mul_f32_e32 v158, v158, v156
	v_mul_f32_e32 v158, 0xbdd2d3e8, v158
	v_mul_f32_e32 v140, v96, v96
	v_mul_f32_e32 v141, v97, v97
	v_mul_f32_e32 v142, v98, v98
	v_mul_f32_e32 v143, v99, v99
	v_mul_f32_e32 v144, v92, v92
	v_mul_f32_e32 v145, v93, v93
	v_mul_f32_e32 v146, v94, v94
	v_mul_f32_e32 v147, v95, v95
	v_mul_f32_e32 v148, v88, v88
	v_mul_f32_e32 v149, v89, v89
	v_mul_f32_e32 v150, v90, v90
	v_mul_f32_e32 v151, v91, v91
	v_mul_f32_e32 v152, v84, v84
	v_mul_f32_e32 v153, v85, v85
	v_mul_f32_e32 v154, v86, v86
	v_mul_f32_e32 v155, v87, v87
	v_fma_f32 v140, v140, v158, v157
	v_fma_f32 v141, v141, v158, v157
	v_fma_f32 v142, v142, v158, v157
	v_fma_f32 v143, v143, v158, v157
	v_fma_f32 v144, v144, v158, v157
	v_fma_f32 v145, v145, v158, v157
	v_fma_f32 v146, v146, v158, v157
	v_fma_f32 v147, v147, v158, v157
	v_fma_f32 v148, v148, v158, v157
	v_fma_f32 v149, v149, v158, v157
	v_fma_f32 v150, v150, v158, v157
	v_fma_f32 v151, v151, v158, v157
	v_fma_f32 v152, v152, v158, v157
	v_fma_f32 v153, v153, v158, v157
	v_fma_f32 v154, v154, v158, v157
	v_fma_f32 v155, v155, v158, v157
	v_mul_f32_e32 v140, v96, v140
	v_mul_f32_e32 v141, v97, v141
	v_mul_f32_e32 v142, v98, v142
	v_mul_f32_e32 v143, v99, v143
	v_mul_f32_e32 v144, v92, v144
	v_mul_f32_e32 v145, v93, v145
	v_mul_f32_e32 v146, v94, v146
	v_mul_f32_e32 v147, v95, v147
	v_mul_f32_e32 v148, v88, v148
	v_mul_f32_e32 v149, v89, v149
	v_mul_f32_e32 v150, v90, v150
	v_mul_f32_e32 v151, v91, v151
	v_mul_f32_e32 v152, v84, v152
	v_mul_f32_e32 v153, v85, v153
	v_mul_f32_e32 v154, v86, v154
	v_mul_f32_e32 v155, v87, v155
	v_exp_f32_e32 v140, v140
	v_exp_f32_e32 v141, v141
	v_exp_f32_e32 v142, v142
	v_exp_f32_e32 v143, v143
	v_exp_f32_e32 v144, v144
	v_exp_f32_e32 v145, v145
	v_exp_f32_e32 v146, v146
	v_exp_f32_e32 v147, v147
	v_exp_f32_e32 v148, v148
	v_exp_f32_e32 v149, v149
	v_exp_f32_e32 v150, v150
	v_exp_f32_e32 v151, v151
	v_exp_f32_e32 v152, v152
	v_exp_f32_e32 v153, v153
	v_exp_f32_e32 v154, v154
	v_exp_f32_e32 v155, v155
	v_fma_f32 v140, v140, v159, v159
	v_fma_f32 v141, v141, v159, v159
	v_fma_f32 v142, v142, v159, v159
	v_fma_f32 v143, v143, v159, v159
	v_fma_f32 v144, v144, v159, v159
	v_fma_f32 v145, v145, v159, v159
	v_fma_f32 v146, v146, v159, v159
	v_fma_f32 v147, v147, v159, v159
	v_fma_f32 v148, v148, v159, v159
	v_fma_f32 v149, v149, v159, v159
	v_fma_f32 v150, v150, v159, v159
	v_fma_f32 v151, v151, v159, v159
	v_fma_f32 v152, v152, v159, v159
	v_fma_f32 v153, v153, v159, v159
	v_fma_f32 v154, v154, v159, v159
	v_fma_f32 v155, v155, v159, v159
	v_rcp_f32_e32 v140, v140
	v_rcp_f32_e32 v141, v141
	v_rcp_f32_e32 v142, v142
	v_rcp_f32_e32 v143, v143
	v_rcp_f32_e32 v144, v144
	v_rcp_f32_e32 v145, v145
	v_rcp_f32_e32 v146, v146
	v_rcp_f32_e32 v147, v147
	v_rcp_f32_e32 v148, v148
	v_rcp_f32_e32 v149, v149
	v_rcp_f32_e32 v150, v150
	v_rcp_f32_e32 v151, v151
	v_rcp_f32_e32 v152, v152
	v_rcp_f32_e32 v153, v153
	v_rcp_f32_e32 v154, v154
	v_rcp_f32_e32 v155, v155
	v_mul_f32_e32 v96, v96, v140
	v_mul_f32_e32 v97, v97, v141
	v_mul_f32_e32 v98, v98, v142
	v_mul_f32_e32 v99, v99, v143
	v_mul_f32_e32 v92, v92, v144
	v_mul_f32_e32 v93, v93, v145
	v_mul_f32_e32 v94, v94, v146
	v_mul_f32_e32 v95, v95, v147
	v_mul_f32_e32 v88, v88, v148
	v_mul_f32_e32 v89, v89, v149
	v_mul_f32_e32 v90, v90, v150
	v_mul_f32_e32 v91, v91, v151
	v_mul_f32_e32 v84, v84, v152
	v_mul_f32_e32 v85, v85, v153
	v_mul_f32_e32 v86, v86, v154
	v_mul_f32_e32 v87, v87, v155
	s_mov_b64 s[0:1], 0x8000
	v_lshl_add_u64 v[136:137], v[134:135], 0, s[0:1]
	v_cvt_pk_bf16_f32 v96, v96, v97
	v_cvt_pk_bf16_f32 v97, v98, v99
	v_cvt_pk_bf16_f32 v98, v92, v93
	v_cvt_pk_bf16_f32 v99, v94, v95
	global_store_dwordx4 v[136:137], v[96:99], off
	v_cvt_pk_bf16_f32 v88, v88, v89
	v_cvt_pk_bf16_f32 v89, v90, v91
	v_cvt_pk_bf16_f32 v90, v84, v85
	v_cvt_pk_bf16_f32 v91, v86, v87
	global_store_dwordx4 v[136:137], v[88:91], off offset:256
	s_waitcnt lgkmcnt(0)
	v_mov_b32_e32 v156, v160
	ds_read_b32 v160, v205 offset:512
	v_mul_f32_e32 v158, v156, v156
	v_mul_f32_e32 v157, 0xc0135761, v156
	v_rcp_f32_e32 v159, v156
	v_mul_f32_e32 v158, v158, v156
	v_mul_f32_e32 v158, 0xbdd2d3e8, v158
	v_mul_f32_e32 v140, v80, v80
	v_mul_f32_e32 v141, v81, v81
	v_mul_f32_e32 v142, v82, v82
	v_mul_f32_e32 v143, v83, v83
	v_mul_f32_e32 v144, v76, v76
	v_mul_f32_e32 v145, v77, v77
	v_mul_f32_e32 v146, v78, v78
	v_mul_f32_e32 v147, v79, v79
	v_mul_f32_e32 v148, v72, v72
	v_mul_f32_e32 v149, v73, v73
	v_mul_f32_e32 v150, v74, v74
	v_mul_f32_e32 v151, v75, v75
	v_mul_f32_e32 v152, v68, v68
	v_mul_f32_e32 v153, v69, v69
	v_mul_f32_e32 v154, v70, v70
	v_mul_f32_e32 v155, v71, v71
	v_fma_f32 v140, v140, v158, v157
	v_fma_f32 v141, v141, v158, v157
	v_fma_f32 v142, v142, v158, v157
	v_fma_f32 v143, v143, v158, v157
	v_fma_f32 v144, v144, v158, v157
	v_fma_f32 v145, v145, v158, v157
	v_fma_f32 v146, v146, v158, v157
	v_fma_f32 v147, v147, v158, v157
	v_fma_f32 v148, v148, v158, v157
	v_fma_f32 v149, v149, v158, v157
	v_fma_f32 v150, v150, v158, v157
	v_fma_f32 v151, v151, v158, v157
	v_fma_f32 v152, v152, v158, v157
	v_fma_f32 v153, v153, v158, v157
	v_fma_f32 v154, v154, v158, v157
	v_fma_f32 v155, v155, v158, v157
	v_mul_f32_e32 v140, v80, v140
	v_mul_f32_e32 v141, v81, v141
	v_mul_f32_e32 v142, v82, v142
	v_mul_f32_e32 v143, v83, v143
	v_mul_f32_e32 v144, v76, v144
	v_mul_f32_e32 v145, v77, v145
	v_mul_f32_e32 v146, v78, v146
	v_mul_f32_e32 v147, v79, v147
	v_mul_f32_e32 v148, v72, v148
	v_mul_f32_e32 v149, v73, v149
; __device__ __forceinline__ u32x4 pack8(const f32x4 a, const f32x4 b) { u32x4 w; w.x = cvt_pk_bf16(a[0], a[1]); w.y = cvt_pk_bf16(a[2], a[3]); w.z = cvt_pk_bf16(b[0], b[1]); w.w = cvt_pk_bf16(b[2], b[3]); return w; }
;     const float c0 = act == 1 ? -2.302208198f : -1.4426950408889634f, c1 = act == 1 ? -0.10294324f : 0.f;
; #pragma unroll
;     for (int ai = 0; ai < 2; ++ai) { if (ai == 1 && halfunit) break;
; #pragma unroll
;         for (int m = 0; m < 4; ++m) { bf16_t* rowp = base + (size_t)(row0 + ai * HALF + m * 16) * ldc + col0; float ls1 = 0.f, ls2 = 0.f; const float rf = rsr[ai * HALF + m * 16];
; #pragma unroll
;             for (int bj = 0; bj < 2; ++bj) { f32x4 v0 = acc[ai][bj][m][0] * rf, v1 = acc[ai][bj][m][1] * rf;
;                 if (act != 0) {
; #pragma unroll
;                     for (int e = 0; e < 4; ++e) { const float x0 = v0[e], x1 = v1[e];
;                         const float r0 = __builtin_amdgcn_rcpf(1.0f + __builtin_amdgcn_exp2f(x0 * (c0 + c1 * x0 * x0))), r1 = __builtin_amdgcn_rcpf(1.0f + __builtin_amdgcn_exp2f(x1 * (c0 + c1 * x1 * x1)));
;                         v0[e] = act == 1 ? x0 * r0 : r0; v1[e] = act == 1 ? x1 * r1 : r1; } }
;                 if (stat) {
; #pragma unroll
;                     for (int e = 0; e < 4; ++e) { ls1 += v0[e] + v1[e]; ls2 += v0[e] * v0[e] + v1[e] * v1[e]; } }
;                 *(u32x4*)(rowp + bj * HALF) = pack8(v0, v1); }
	v_mul_f32_e32 v150, v74, v150
	v_mul_f32_e32 v151, v75, v151
	v_mul_f32_e32 v152, v68, v152
	v_mul_f32_e32 v153, v69, v153
	v_mul_f32_e32 v154, v70, v154
	v_mul_f32_e32 v155, v71, v155
	v_exp_f32_e32 v140, v140
	v_exp_f32_e32 v141, v141
	v_exp_f32_e32 v142, v142
	v_exp_f32_e32 v143, v143
	v_exp_f32_e32 v144, v144
	v_exp_f32_e32 v145, v145
	v_exp_f32_e32 v146, v146
	v_exp_f32_e32 v147, v147
	v_exp_f32_e32 v148, v148
	v_exp_f32_e32 v149, v149
	v_exp_f32_e32 v150, v150
	v_exp_f32_e32 v151, v151
	v_exp_f32_e32 v152, v152
	v_exp_f32_e32 v153, v153
	v_exp_f32_e32 v154, v154
	v_exp_f32_e32 v155, v155
	v_fma_f32 v140, v140, v159, v159
	v_fma_f32 v141, v141, v159, v159
	v_fma_f32 v142, v142, v159, v159
	v_fma_f32 v143, v143, v159, v159
	v_fma_f32 v144, v144, v159, v159
	v_fma_f32 v145, v145, v159, v159
	v_fma_f32 v146, v146, v159, v159
	v_fma_f32 v147, v147, v159, v159
	v_fma_f32 v148, v148, v159, v159
	v_fma_f32 v149, v149, v159, v159
	v_fma_f32 v150, v150, v159, v159
	v_fma_f32 v151, v151, v159, v159
	v_fma_f32 v152, v152, v159, v159
	v_fma_f32 v153, v153, v159, v159
	v_fma_f32 v154, v154, v159, v159
	v_fma_f32 v155, v155, v159, v159
	v_rcp_f32_e32 v140, v140
	v_rcp_f32_e32 v141, v141
	v_rcp_f32_e32 v142, v142
	v_rcp_f32_e32 v143, v143
	v_rcp_f32_e32 v144, v144
	v_rcp_f32_e32 v145, v145
	v_rcp_f32_e32 v146, v146
	v_rcp_f32_e32 v147, v147
	v_rcp_f32_e32 v148, v148
	v_rcp_f32_e32 v149, v149
	v_rcp_f32_e32 v150, v150
	v_rcp_f32_e32 v151, v151
	v_rcp_f32_e32 v152, v152
	v_rcp_f32_e32 v153, v153
	v_rcp_f32_e32 v154, v154
	v_rcp_f32_e32 v155, v155
	v_mul_f32_e32 v80, v80, v140
	v_mul_f32_e32 v81, v81, v141
	v_mul_f32_e32 v82, v82, v142
	v_mul_f32_e32 v83, v83, v143
	v_mul_f32_e32 v76, v76, v144
	v_mul_f32_e32 v77, v77, v145
	v_mul_f32_e32 v78, v78, v146
	v_mul_f32_e32 v79, v79, v147
	v_mul_f32_e32 v72, v72, v148
	v_mul_f32_e32 v73, v73, v149
	v_mul_f32_e32 v74, v74, v150
	v_mul_f32_e32 v75, v75, v151
	v_mul_f32_e32 v68, v68, v152
	v_mul_f32_e32 v69, v69, v153
	v_mul_f32_e32 v70, v70, v154
	v_mul_f32_e32 v71, v71, v155
	s_mov_b64 s[0:1], 0xc000
	v_lshl_add_u64 v[136:137], v[134:135], 0, s[0:1]
	v_cvt_pk_bf16_f32 v80, v80, v81
	v_cvt_pk_bf16_f32 v81, v82, v83
	v_cvt_pk_bf16_f32 v82, v76, v77
	v_cvt_pk_bf16_f32 v83, v78, v79
	global_store_dwordx4 v[136:137], v[80:83], off
	v_cvt_pk_bf16_f32 v72, v72, v73
	v_cvt_pk_bf16_f32 v73, v74, v75
	v_cvt_pk_bf16_f32 v74, v68, v69
	v_cvt_pk_bf16_f32 v75, v70, v71
	global_store_dwordx4 v[136:137], v[72:75], off offset:256
	s_waitcnt lgkmcnt(0)
	v_mov_b32_e32 v156, v160
	ds_read_b32 v160, v205 offset:576
	v_mul_f32_e32 v158, v156, v156
	v_mul_f32_e32 v157, 0xc0135761, v156
	v_rcp_f32_e32 v159, v156
	v_mul_f32_e32 v158, v158, v156
	v_mul_f32_e32 v158, 0xbdd2d3e8, v158
	v_mul_f32_e32 v140, v64, v64
	v_mul_f32_e32 v141, v65, v65
	v_mul_f32_e32 v142, v66, v66
	v_mul_f32_e32 v143, v67, v67
	v_mul_f32_e32 v144, v60, v60
	v_mul_f32_e32 v145, v61, v61
	v_mul_f32_e32 v146, v62, v62
	v_mul_f32_e32 v147, v63, v63
	v_mul_f32_e32 v148, v56, v56
	v_mul_f32_e32 v149, v57, v57
	v_mul_f32_e32 v150, v58, v58
	v_mul_f32_e32 v151, v59, v59
	v_mul_f32_e32 v152, v52, v52
	v_mul_f32_e32 v153, v53, v53
	v_mul_f32_e32 v154, v54, v54
	v_mul_f32_e32 v155, v55, v55
	v_fma_f32 v140, v140, v158, v157
	v_fma_f32 v141, v141, v158, v157
	v_fma_f32 v142, v142, v158, v157
	v_fma_f32 v143, v143, v158, v157
	v_fma_f32 v144, v144, v158, v157
	v_fma_f32 v145, v145, v158, v157
	v_fma_f32 v146, v146, v158, v157
	v_fma_f32 v147, v147, v158, v157
	v_fma_f32 v148, v148, v158, v157
	v_fma_f32 v149, v149, v158, v157
	v_fma_f32 v150, v150, v158, v157
	v_fma_f32 v151, v151, v158, v157
	v_fma_f32 v152, v152, v158, v157
	v_fma_f32 v153, v153, v158, v157
	v_fma_f32 v154, v154, v158, v157
	v_fma_f32 v155, v155, v158, v157
	v_mul_f32_e32 v140, v64, v140
	v_mul_f32_e32 v141, v65, v141
	v_mul_f32_e32 v142, v66, v142
	v_mul_f32_e32 v143, v67, v143
	v_mul_f32_e32 v144, v60, v144
	v_mul_f32_e32 v145, v61, v145
	v_mul_f32_e32 v146, v62, v146
	v_mul_f32_e32 v147, v63, v147
	v_mul_f32_e32 v148, v56, v148
	v_mul_f32_e32 v149, v57, v149
	v_mul_f32_e32 v150, v58, v150
	v_mul_f32_e32 v151, v59, v151
	v_mul_f32_e32 v152, v52, v152
	v_mul_f32_e32 v153, v53, v153
	v_mul_f32_e32 v154, v54, v154
	v_mul_f32_e32 v155, v55, v155
	v_exp_f32_e32 v140, v140
	v_exp_f32_e32 v141, v141
	v_exp_f32_e32 v142, v142
	v_exp_f32_e32 v143, v143
	v_exp_f32_e32 v144, v144
	v_exp_f32_e32 v145, v145
	v_exp_f32_e32 v146, v146
	v_exp_f32_e32 v147, v147
	v_exp_f32_e32 v148, v148
	v_exp_f32_e32 v149, v149
	v_exp_f32_e32 v150, v150
	v_exp_f32_e32 v151, v151
	v_exp_f32_e32 v152, v152
	v_exp_f32_e32 v153, v153
	v_exp_f32_e32 v154, v154
	v_exp_f32_e32 v155, v155
	v_fma_f32 v140, v140, v159, v159
	v_fma_f32 v141, v141, v159, v159
	v_fma_f32 v142, v142, v159, v159
	v_fma_f32 v143, v143, v159, v159
	v_fma_f32 v144, v144, v159, v159
	v_fma_f32 v145, v145, v159, v159
	v_fma_f32 v146, v146, v159, v159
	v_fma_f32 v147, v147, v159, v159
	v_fma_f32 v148, v148, v159, v159
	v_fma_f32 v149, v149, v159, v159
	v_fma_f32 v150, v150, v159, v159
	v_fma_f32 v151, v151, v159, v159
	v_fma_f32 v152, v152, v159, v159
	v_fma_f32 v153, v153, v159, v159
	v_fma_f32 v154, v154, v159, v159
	v_fma_f32 v155, v155, v159, v159
	v_rcp_f32_e32 v140, v140
	v_rcp_f32_e32 v141, v141
	v_rcp_f32_e32 v142, v142
	v_rcp_f32_e32 v143, v143
	v_rcp_f32_e32 v144, v144
	v_rcp_f32_e32 v145, v145
	v_rcp_f32_e32 v146, v146
	v_rcp_f32_e32 v147, v147
	v_rcp_f32_e32 v148, v148
	v_rcp_f32_e32 v149, v149
	v_rcp_f32_e32 v150, v150
	v_rcp_f32_e32 v151, v151
	v_rcp_f32_e32 v152, v152
	v_rcp_f32_e32 v153, v153
	v_rcp_f32_e32 v154, v154
	v_rcp_f32_e32 v155, v155
	v_mul_f32_e32 v64, v64, v140
	v_mul_f32_e32 v65, v65, v141
	v_mul_f32_e32 v66, v66, v142
	v_mul_f32_e32 v67, v67, v143
	v_mul_f32_e32 v60, v60, v144
	v_mul_f32_e32 v61, v61, v145
	v_mul_f32_e32 v62, v62, v146
	v_mul_f32_e32 v63, v63, v147
	v_mul_f32_e32 v56, v56, v148
	v_mul_f32_e32 v57, v57, v149
	v_mul_f32_e32 v58, v58, v150
	v_mul_f32_e32 v59, v59, v151
	v_mul_f32_e32 v52, v52, v152
	v_mul_f32_e32 v53, v53, v153
	v_mul_f32_e32 v54, v54, v154
	v_mul_f32_e32 v55, v55, v155
	s_mov_b64 s[0:1], 0x20000
	v_lshl_add_u64 v[136:137], v[134:135], 0, s[0:1]
	v_cvt_pk_bf16_f32 v64, v64, v65
	v_cvt_pk_bf16_f32 v65, v66, v67
	v_cvt_pk_bf16_f32 v66, v60, v61
	v_cvt_pk_bf16_f32 v67, v62, v63
	global_store_dwordx4 v[136:137], v[64:67], off
	v_cvt_pk_bf16_f32 v56, v56, v57
	v_cvt_pk_bf16_f32 v57, v58, v59
	v_cvt_pk_bf16_f32 v58, v52, v53
	v_cvt_pk_bf16_f32 v59, v54, v55
	global_store_dwordx4 v[136:137], v[56:59], off offset:256
	s_waitcnt lgkmcnt(0)
; __device__ __forceinline__ u32x4 pack8(const f32x4 a, const f32x4 b) { u32x4 w; w.x = cvt_pk_bf16(a[0], a[1]); w.y = cvt_pk_bf16(a[2], a[3]); w.z = cvt_pk_bf16(b[0], b[1]); w.w = cvt_pk_bf16(b[2], b[3]); return w; }
;     const float c0 = act == 1 ? -2.302208198f : -1.4426950408889634f, c1 = act == 1 ? -0.10294324f : 0.f;
; #pragma unroll
;     for (int ai = 0; ai < 2; ++ai) { if (ai == 1 && halfunit) break;
; #pragma unroll
;         for (int m = 0; m < 4; ++m) { bf16_t* rowp = base + (size_t)(row0 + ai * HALF + m * 16) * ldc + col0; float ls1 = 0.f, ls2 = 0.f; const float rf = rsr[ai * HALF + m * 16];
; #pragma unroll
;             for (int bj = 0; bj < 2; ++bj) { f32x4 v0 = acc[ai][bj][m][0] * rf, v1 = acc[ai][bj][m][1] * rf;
;                 if (act != 0) {
; #pragma unroll
;                     for (int e = 0; e < 4; ++e) { const float x0 = v0[e], x1 = v1[e];
;                         const float r0 = __builtin_amdgcn_rcpf(1.0f + __builtin_amdgcn_exp2f(x0 * (c0 + c1 * x0 * x0))), r1 = __builtin_amdgcn_rcpf(1.0f + __builtin_amdgcn_exp2f(x1 * (c0 + c1 * x1 * x1)));
;                         v0[e] = act == 1 ? x0 * r0 : r0; v1[e] = act == 1 ? x1 * r1 : r1; } }
;                 if (stat) {
; #pragma unroll
;                     for (int e = 0; e < 4; ++e) { ls1 += v0[e] + v1[e]; ls2 += v0[e] * v0[e] + v1[e] * v1[e]; } }
;                 *(u32x4*)(rowp + bj * HALF) = pack8(v0, v1); }
	v_mov_b32_e32 v156, v160
	ds_read_b32 v160, v205 offset:640
	v_mul_f32_e32 v158, v156, v156
	v_mul_f32_e32 v157, 0xc0135761, v156
	v_rcp_f32_e32 v159, v156
	v_mul_f32_e32 v158, v158, v156
	v_mul_f32_e32 v158, 0xbdd2d3e8, v158
	v_mul_f32_e32 v140, v48, v48
	v_mul_f32_e32 v141, v49, v49
	v_mul_f32_e32 v142, v50, v50
	v_mul_f32_e32 v143, v51, v51
	v_mul_f32_e32 v144, v44, v44
	v_mul_f32_e32 v145, v45, v45
	v_mul_f32_e32 v146, v46, v46
	v_mul_f32_e32 v147, v47, v47
	v_mul_f32_e32 v148, v40, v40
	v_mul_f32_e32 v149, v41, v41
	v_mul_f32_e32 v150, v42, v42
	v_mul_f32_e32 v151, v43, v43
	v_mul_f32_e32 v152, v36, v36
	v_mul_f32_e32 v153, v37, v37
	v_mul_f32_e32 v154, v38, v38
	v_mul_f32_e32 v155, v39, v39
	v_fma_f32 v140, v140, v158, v157
	v_fma_f32 v141, v141, v158, v157
	v_fma_f32 v142, v142, v158, v157
	v_fma_f32 v143, v143, v158, v157
	v_fma_f32 v144, v144, v158, v157
	v_fma_f32 v145, v145, v158, v157
	v_fma_f32 v146, v146, v158, v157
	v_fma_f32 v147, v147, v158, v157
	v_fma_f32 v148, v148, v158, v157
	v_fma_f32 v149, v149, v158, v157
	v_fma_f32 v150, v150, v158, v157
	v_fma_f32 v151, v151, v158, v157
	v_fma_f32 v152, v152, v158, v157
	v_fma_f32 v153, v153, v158, v157
	v_fma_f32 v154, v154, v158, v157
	v_fma_f32 v155, v155, v158, v157
	v_mul_f32_e32 v140, v48, v140
	v_mul_f32_e32 v141, v49, v141
	v_mul_f32_e32 v142, v50, v142
	v_mul_f32_e32 v143, v51, v143
	v_mul_f32_e32 v144, v44, v144
	v_mul_f32_e32 v145, v45, v145
	v_mul_f32_e32 v146, v46, v146
	v_mul_f32_e32 v147, v47, v147
	v_mul_f32_e32 v148, v40, v148
	v_mul_f32_e32 v149, v41, v149
	v_mul_f32_e32 v150, v42, v150
	v_mul_f32_e32 v151, v43, v151
	v_mul_f32_e32 v152, v36, v152
	v_mul_f32_e32 v153, v37, v153
	v_mul_f32_e32 v154, v38, v154
	v_mul_f32_e32 v155, v39, v155
	v_exp_f32_e32 v140, v140
	v_exp_f32_e32 v141, v141
	v_exp_f32_e32 v142, v142
	v_exp_f32_e32 v143, v143
	v_exp_f32_e32 v144, v144
	v_exp_f32_e32 v145, v145
	v_exp_f32_e32 v146, v146
	v_exp_f32_e32 v147, v147
	v_exp_f32_e32 v148, v148
	v_exp_f32_e32 v149, v149
	v_exp_f32_e32 v150, v150
	v_exp_f32_e32 v151, v151
	v_exp_f32_e32 v152, v152
	v_exp_f32_e32 v153, v153
	v_exp_f32_e32 v154, v154
	v_exp_f32_e32 v155, v155
	v_fma_f32 v140, v140, v159, v159
	v_fma_f32 v141, v141, v159, v159
	v_fma_f32 v142, v142, v159, v159
	v_fma_f32 v143, v143, v159, v159
	v_fma_f32 v144, v144, v159, v159
	v_fma_f32 v145, v145, v159, v159
	v_fma_f32 v146, v146, v159, v159
	v_fma_f32 v147, v147, v159, v159
	v_fma_f32 v148, v148, v159, v159
	v_fma_f32 v149, v149, v159, v159
	v_fma_f32 v150, v150, v159, v159
	v_fma_f32 v151, v151, v159, v159
	v_fma_f32 v152, v152, v159, v159
	v_fma_f32 v153, v153, v159, v159
	v_fma_f32 v154, v154, v159, v159
	v_fma_f32 v155, v155, v159, v159
	v_rcp_f32_e32 v140, v140
	v_rcp_f32_e32 v141, v141
	v_rcp_f32_e32 v142, v142
	v_rcp_f32_e32 v143, v143
	v_rcp_f32_e32 v144, v144
	v_rcp_f32_e32 v145, v145
	v_rcp_f32_e32 v146, v146
	v_rcp_f32_e32 v147, v147
	v_rcp_f32_e32 v148, v148
	v_rcp_f32_e32 v149, v149
	v_rcp_f32_e32 v150, v150
	v_rcp_f32_e32 v151, v151
	v_rcp_f32_e32 v152, v152
	v_rcp_f32_e32 v153, v153
	v_rcp_f32_e32 v154, v154
	v_rcp_f32_e32 v155, v155
	v_mul_f32_e32 v48, v48, v140
	v_mul_f32_e32 v49, v49, v141
	v_mul_f32_e32 v50, v50, v142
	v_mul_f32_e32 v51, v51, v143
	v_mul_f32_e32 v44, v44, v144
	v_mul_f32_e32 v45, v45, v145
	v_mul_f32_e32 v46, v46, v146
	v_mul_f32_e32 v47, v47, v147
	v_mul_f32_e32 v40, v40, v148
	v_mul_f32_e32 v41, v41, v149
	v_mul_f32_e32 v42, v42, v150
	v_mul_f32_e32 v43, v43, v151
	v_mul_f32_e32 v36, v36, v152
	v_mul_f32_e32 v37, v37, v153
	v_mul_f32_e32 v38, v38, v154
	v_mul_f32_e32 v39, v39, v155
	s_mov_b64 s[0:1], 0x24000
	v_lshl_add_u64 v[136:137], v[134:135], 0, s[0:1]
	v_cvt_pk_bf16_f32 v48, v48, v49
	v_cvt_pk_bf16_f32 v49, v50, v51
	v_cvt_pk_bf16_f32 v50, v44, v45
	v_cvt_pk_bf16_f32 v51, v46, v47
	global_store_dwordx4 v[136:137], v[48:51], off
	v_cvt_pk_bf16_f32 v40, v40, v41
	v_cvt_pk_bf16_f32 v41, v42, v43
	v_cvt_pk_bf16_f32 v42, v36, v37
	v_cvt_pk_bf16_f32 v43, v38, v39
	global_store_dwordx4 v[136:137], v[40:43], off offset:256
	s_waitcnt lgkmcnt(0)
	v_mov_b32_e32 v156, v160
	ds_read_b32 v160, v205 offset:704
	v_mul_f32_e32 v158, v156, v156
	v_mul_f32_e32 v157, 0xc0135761, v156
	v_rcp_f32_e32 v159, v156
	v_mul_f32_e32 v158, v158, v156
	v_mul_f32_e32 v158, 0xbdd2d3e8, v158
	v_mul_f32_e32 v140, v32, v32
	v_mul_f32_e32 v141, v33, v33
	v_mul_f32_e32 v142, v34, v34
	v_mul_f32_e32 v143, v35, v35
	v_mul_f32_e32 v144, v28, v28
	v_mul_f32_e32 v145, v29, v29
	v_mul_f32_e32 v146, v30, v30
	v_mul_f32_e32 v147, v31, v31
	v_mul_f32_e32 v148, v24, v24
	v_mul_f32_e32 v149, v25, v25
	v_mul_f32_e32 v150, v26, v26
	v_mul_f32_e32 v151, v27, v27
	v_mul_f32_e32 v152, v20, v20
	v_mul_f32_e32 v153, v21, v21
	v_mul_f32_e32 v154, v22, v22
	v_mul_f32_e32 v155, v23, v23
	v_fma_f32 v140, v140, v158, v157
	v_fma_f32 v141, v141, v158, v157
	v_fma_f32 v142, v142, v158, v157
	v_fma_f32 v143, v143, v158, v157
	v_fma_f32 v144, v144, v158, v157
	v_fma_f32 v145, v145, v158, v157
	v_fma_f32 v146, v146, v158, v157
	v_fma_f32 v147, v147, v158, v157
	v_fma_f32 v148, v148, v158, v157
	v_fma_f32 v149, v149, v158, v157
	v_fma_f32 v150, v150, v158, v157
	v_fma_f32 v151, v151, v158, v157
	v_fma_f32 v152, v152, v158, v157
	v_fma_f32 v153, v153, v158, v157
	v_fma_f32 v154, v154, v158, v157
	v_fma_f32 v155, v155, v158, v157
	v_mul_f32_e32 v140, v32, v140
	v_mul_f32_e32 v141, v33, v141
	v_mul_f32_e32 v142, v34, v142
	v_mul_f32_e32 v143, v35, v143
	v_mul_f32_e32 v144, v28, v144
	v_mul_f32_e32 v145, v29, v145
	v_mul_f32_e32 v146, v30, v146
	v_mul_f32_e32 v147, v31, v147
	v_mul_f32_e32 v148, v24, v148
	v_mul_f32_e32 v149, v25, v149
; __device__ __forceinline__ u32x4 pack8(const f32x4 a, const f32x4 b) { u32x4 w; w.x = cvt_pk_bf16(a[0], a[1]); w.y = cvt_pk_bf16(a[2], a[3]); w.z = cvt_pk_bf16(b[0], b[1]); w.w = cvt_pk_bf16(b[2], b[3]); return w; }
;     const float c0 = act == 1 ? -2.302208198f : -1.4426950408889634f, c1 = act == 1 ? -0.10294324f : 0.f;
; #pragma unroll
;     for (int ai = 0; ai < 2; ++ai) { if (ai == 1 && halfunit) break;
; #pragma unroll
;         for (int m = 0; m < 4; ++m) { bf16_t* rowp = base + (size_t)(row0 + ai * HALF + m * 16) * ldc + col0; float ls1 = 0.f, ls2 = 0.f; const float rf = rsr[ai * HALF + m * 16];
; #pragma unroll
;             for (int bj = 0; bj < 2; ++bj) { f32x4 v0 = acc[ai][bj][m][0] * rf, v1 = acc[ai][bj][m][1] * rf;
;                 if (act != 0) {
; #pragma unroll
;                     for (int e = 0; e < 4; ++e) { const float x0 = v0[e], x1 = v1[e];
;                         const float r0 = __builtin_amdgcn_rcpf(1.0f + __builtin_amdgcn_exp2f(x0 * (c0 + c1 * x0 * x0))), r1 = __builtin_amdgcn_rcpf(1.0f + __builtin_amdgcn_exp2f(x1 * (c0 + c1 * x1 * x1)));
;                         v0[e] = act == 1 ? x0 * r0 : r0; v1[e] = act == 1 ? x1 * r1 : r1; } }
;                 if (stat) {
; #pragma unroll
;                     for (int e = 0; e < 4; ++e) { ls1 += v0[e] + v1[e]; ls2 += v0[e] * v0[e] + v1[e] * v1[e]; } }
;                 *(u32x4*)(rowp + bj * HALF) = pack8(v0, v1); }
	v_mul_f32_e32 v150, v26, v150
	v_mul_f32_e32 v151, v27, v151
	v_mul_f32_e32 v152, v20, v152
	v_mul_f32_e32 v153, v21, v153
	v_mul_f32_e32 v154, v22, v154
	v_mul_f32_e32 v155, v23, v155
	v_exp_f32_e32 v140, v140
	v_exp_f32_e32 v141, v141
	v_exp_f32_e32 v142, v142
	v_exp_f32_e32 v143, v143
	v_exp_f32_e32 v144, v144
	v_exp_f32_e32 v145, v145
	v_exp_f32_e32 v146, v146
	v_exp_f32_e32 v147, v147
	v_exp_f32_e32 v148, v148
	v_exp_f32_e32 v149, v149
	v_exp_f32_e32 v150, v150
	v_exp_f32_e32 v151, v151
	v_exp_f32_e32 v152, v152
	v_exp_f32_e32 v153, v153
	v_exp_f32_e32 v154, v154
	v_exp_f32_e32 v155, v155
	v_fma_f32 v140, v140, v159, v159
	v_fma_f32 v141, v141, v159, v159
	v_fma_f32 v142, v142, v159, v159
	v_fma_f32 v143, v143, v159, v159
	v_fma_f32 v144, v144, v159, v159
	v_fma_f32 v145, v145, v159, v159
	v_fma_f32 v146, v146, v159, v159
	v_fma_f32 v147, v147, v159, v159
	v_fma_f32 v148, v148, v159, v159
	v_fma_f32 v149, v149, v159, v159
	v_fma_f32 v150, v150, v159, v159
	v_fma_f32 v151, v151, v159, v159
	v_fma_f32 v152, v152, v159, v159
	v_fma_f32 v153, v153, v159, v159
	v_fma_f32 v154, v154, v159, v159
	v_fma_f32 v155, v155, v159, v159
	v_rcp_f32_e32 v140, v140
	v_rcp_f32_e32 v141, v141
	v_rcp_f32_e32 v142, v142
	v_rcp_f32_e32 v143, v143
	v_rcp_f32_e32 v144, v144
	v_rcp_f32_e32 v145, v145
	v_rcp_f32_e32 v146, v146
	v_rcp_f32_e32 v147, v147
	v_rcp_f32_e32 v148, v148
	v_rcp_f32_e32 v149, v149
	v_rcp_f32_e32 v150, v150
	v_rcp_f32_e32 v151, v151
	v_rcp_f32_e32 v152, v152
	v_rcp_f32_e32 v153, v153
	v_rcp_f32_e32 v154, v154
	v_rcp_f32_e32 v155, v155
	v_mul_f32_e32 v32, v32, v140
	v_mul_f32_e32 v33, v33, v141
	v_mul_f32_e32 v34, v34, v142
	v_mul_f32_e32 v35, v35, v143
	v_mul_f32_e32 v28, v28, v144
	v_mul_f32_e32 v29, v29, v145
	v_mul_f32_e32 v30, v30, v146
	v_mul_f32_e32 v31, v31, v147
	v_mul_f32_e32 v24, v24, v148
	v_mul_f32_e32 v25, v25, v149
	v_mul_f32_e32 v26, v26, v150
	v_mul_f32_e32 v27, v27, v151
	v_mul_f32_e32 v20, v20, v152
	v_mul_f32_e32 v21, v21, v153
	v_mul_f32_e32 v22, v22, v154
	v_mul_f32_e32 v23, v23, v155
	s_mov_b64 s[0:1], 0x28000
	v_lshl_add_u64 v[136:137], v[134:135], 0, s[0:1]
	v_cvt_pk_bf16_f32 v32, v32, v33
	v_cvt_pk_bf16_f32 v33, v34, v35
	v_cvt_pk_bf16_f32 v34, v28, v29
	v_cvt_pk_bf16_f32 v35, v30, v31
	global_store_dwordx4 v[136:137], v[32:35], off
	v_cvt_pk_bf16_f32 v24, v24, v25
	v_cvt_pk_bf16_f32 v25, v26, v27
	v_cvt_pk_bf16_f32 v26, v20, v21
	v_cvt_pk_bf16_f32 v27, v22, v23
	global_store_dwordx4 v[136:137], v[24:27], off offset:256
	s_waitcnt lgkmcnt(0)
	v_mov_b32_e32 v156, v160
	v_mul_f32_e32 v158, v156, v156
	v_mul_f32_e32 v157, 0xc0135761, v156
	v_rcp_f32_e32 v159, v156
	v_mul_f32_e32 v158, v158, v156
	v_mul_f32_e32 v158, 0xbdd2d3e8, v158
	v_mul_f32_e32 v140, v16, v16
	v_mul_f32_e32 v141, v17, v17
	v_mul_f32_e32 v142, v18, v18
	v_mul_f32_e32 v143, v19, v19
	v_mul_f32_e32 v144, v12, v12
	v_mul_f32_e32 v145, v13, v13
	v_mul_f32_e32 v146, v14, v14
	v_mul_f32_e32 v147, v15, v15
	v_mul_f32_e32 v148, v8, v8
	v_mul_f32_e32 v149, v9, v9
	v_mul_f32_e32 v150, v10, v10
	v_mul_f32_e32 v151, v11, v11
	v_mul_f32_e32 v152, v4, v4
	v_mul_f32_e32 v153, v5, v5
	v_mul_f32_e32 v154, v6, v6
	v_mul_f32_e32 v155, v7, v7
	v_fma_f32 v140, v140, v158, v157
	v_fma_f32 v141, v141, v158, v157
	v_fma_f32 v142, v142, v158, v157
	v_fma_f32 v143, v143, v158, v157
	v_fma_f32 v144, v144, v158, v157
	v_fma_f32 v145, v145, v158, v157
	v_fma_f32 v146, v146, v158, v157
	v_fma_f32 v147, v147, v158, v157
	v_fma_f32 v148, v148, v158, v157
	v_fma_f32 v149, v149, v158, v157
	v_fma_f32 v150, v150, v158, v157
	v_fma_f32 v151, v151, v158, v157
	v_fma_f32 v152, v152, v158, v157
	v_fma_f32 v153, v153, v158, v157
	v_fma_f32 v154, v154, v158, v157
	v_fma_f32 v155, v155, v158, v157
	v_mul_f32_e32 v140, v16, v140
	v_mul_f32_e32 v141, v17, v141
	v_mul_f32_e32 v142, v18, v142
	v_mul_f32_e32 v143, v19, v143
	v_mul_f32_e32 v144, v12, v144
	v_mul_f32_e32 v145, v13, v145
	v_mul_f32_e32 v146, v14, v146
	v_mul_f32_e32 v147, v15, v147
	v_mul_f32_e32 v148, v8, v148
	v_mul_f32_e32 v149, v9, v149
	v_mul_f32_e32 v150, v10, v150
	v_mul_f32_e32 v151, v11, v151
	v_mul_f32_e32 v152, v4, v152
	v_mul_f32_e32 v153, v5, v153
	v_mul_f32_e32 v154, v6, v154
	v_mul_f32_e32 v155, v7, v155
	v_exp_f32_e32 v140, v140
	v_exp_f32_e32 v141, v141
	v_exp_f32_e32 v142, v142
	v_exp_f32_e32 v143, v143
	v_exp_f32_e32 v144, v144
	v_exp_f32_e32 v145, v145
	v_exp_f32_e32 v146, v146
	v_exp_f32_e32 v147, v147
	v_exp_f32_e32 v148, v148
	v_exp_f32_e32 v149, v149
	v_exp_f32_e32 v150, v150
	v_exp_f32_e32 v151, v151
	v_exp_f32_e32 v152, v152
	v_exp_f32_e32 v153, v153
	v_exp_f32_e32 v154, v154
	v_exp_f32_e32 v155, v155
	v_fma_f32 v140, v140, v159, v159
	v_fma_f32 v141, v141, v159, v159
	v_fma_f32 v142, v142, v159, v159
	v_fma_f32 v143, v143, v159, v159
	v_fma_f32 v144, v144, v159, v159
	v_fma_f32 v145, v145, v159, v159
	v_fma_f32 v146, v146, v159, v159
	v_fma_f32 v147, v147, v159, v159
	v_fma_f32 v148, v148, v159, v159
	v_fma_f32 v149, v149, v159, v159
	v_fma_f32 v150, v150, v159, v159
	v_fma_f32 v151, v151, v159, v159
	v_fma_f32 v152, v152, v159, v159
	v_fma_f32 v153, v153, v159, v159
	v_fma_f32 v154, v154, v159, v159
	v_fma_f32 v155, v155, v159, v159
	v_rcp_f32_e32 v140, v140
	v_rcp_f32_e32 v141, v141
	v_rcp_f32_e32 v142, v142
	v_rcp_f32_e32 v143, v143
	v_rcp_f32_e32 v144, v144
	v_rcp_f32_e32 v145, v145
	v_rcp_f32_e32 v146, v146
	v_rcp_f32_e32 v147, v147
	v_rcp_f32_e32 v148, v148
	v_rcp_f32_e32 v149, v149
	v_rcp_f32_e32 v150, v150
	v_rcp_f32_e32 v151, v151
	v_rcp_f32_e32 v152, v152
	v_rcp_f32_e32 v153, v153
	v_rcp_f32_e32 v154, v154
	v_rcp_f32_e32 v155, v155
	v_mul_f32_e32 v16, v16, v140
	v_mul_f32_e32 v17, v17, v141
	v_mul_f32_e32 v18, v18, v142
	v_mul_f32_e32 v19, v19, v143
	v_mul_f32_e32 v12, v12, v144
	v_mul_f32_e32 v13, v13, v145
	v_mul_f32_e32 v14, v14, v146
	v_mul_f32_e32 v15, v15, v147
	v_mul_f32_e32 v8, v8, v148
	v_mul_f32_e32 v9, v9, v149
	v_mul_f32_e32 v10, v10, v150
	v_mul_f32_e32 v11, v11, v151
	v_mul_f32_e32 v4, v4, v152
	v_mul_f32_e32 v5, v5, v153
	v_mul_f32_e32 v6, v6, v154
	v_mul_f32_e32 v7, v7, v155
	s_mov_b64 s[0:1], 0x2c000
	v_lshl_add_u64 v[136:137], v[134:135], 0, s[0:1]
	v_cvt_pk_bf16_f32 v16, v16, v17
	v_cvt_pk_bf16_f32 v17, v18, v19
	v_cvt_pk_bf16_f32 v18, v12, v13
	v_cvt_pk_bf16_f32 v19, v14, v15
	global_store_dwordx4 v[136:137], v[16:19], off
	v_cvt_pk_bf16_f32 v8, v8, v9
	v_cvt_pk_bf16_f32 v9, v10, v11
	v_cvt_pk_bf16_f32 v10, v4, v5
	v_cvt_pk_bf16_f32 v11, v6, v7
	global_store_dwordx4 v[136:137], v[8:11], off offset:256
	s_branch .Lt8_end
; __device__ __forceinline__ u32x4 pack8(const f32x4 a, const f32x4 b) { u32x4 w; w.x = cvt_pk_bf16(a[0], a[1]); w.y = cvt_pk_bf16(a[2], a[3]); w.z = cvt_pk_bf16(b[0], b[1]); w.w = cvt_pk_bf16(b[2], b[3]); return w; }
;     const float c0 = act == 1 ? -2.302208198f : -1.4426950408889634f, c1 = act == 1 ? -0.10294324f : 0.f;
; #pragma unroll
;     for (int ai = 0; ai < 2; ++ai) { if (ai == 1 && halfunit) break;
; #pragma unroll
;         for (int m = 0; m < 4; ++m) { bf16_t* rowp = base + (size_t)(row0 + ai * HALF + m * 16) * ldc + col0; float ls1 = 0.f, ls2 = 0.f; const float rf = rsr[ai * HALF + m * 16];
; #pragma unroll
;             for (int bj = 0; bj < 2; ++bj) { f32x4 v0 = acc[ai][bj][m][0] * rf, v1 = acc[ai][bj][m][1] * rf;
;                 if (act != 0) {
; #pragma unroll
;                     for (int e = 0; e < 4; ++e) { const float x0 = v0[e], x1 = v1[e];
;                         const float r0 = __builtin_amdgcn_rcpf(1.0f + __builtin_amdgcn_exp2f(x0 * (c0 + c1 * x0 * x0))), r1 = __builtin_amdgcn_rcpf(1.0f + __builtin_amdgcn_exp2f(x1 * (c0 + c1 * x1 * x1)));
;                         v0[e] = act == 1 ? x0 * r0 : r0; v1[e] = act == 1 ? x1 * r1 : r1; } }
;                 if (stat) {
; #pragma unroll
;                     for (int e = 0; e < 4; ++e) { ls1 += v0[e] + v1[e]; ls2 += v0[e] * v0[e] + v1[e] * v1[e]; } }
;                 *(u32x4*)(rowp + bj * HALF) = pack8(v0, v1); }
;             if (stat) { ls1 = xor_add<16>(ls1); ls1 = xor_add<32>(ls1); ls2 = xor_add<16>(ls2); ls2 = xor_add<32>(ls2);
;                 if (fq == 0) { f32x2 st2; st2.x = ls1; st2.y = ls2; *(f32x2*)(stat + (size_t)(row0 + ai * HALF + m * 16) * 16) = st2; } }
.Lt8_gstat:
	s_waitcnt lgkmcnt(0)
	ds_read_b32 v160, v205 offset:64
	v_mul_f32_e32 v158, v156, v156
	v_mul_f32_e32 v157, 0xc0135761, v156
	v_rcp_f32_e32 v159, v156
	v_mul_f32_e32 v158, v158, v156
	v_mul_f32_e32 v158, 0xbdd2d3e8, v158
	v_mul_f32_e32 v140, v128, v128
	v_mul_f32_e32 v141, v129, v129
	v_mul_f32_e32 v142, v130, v130
	v_mul_f32_e32 v143, v131, v131
	v_mul_f32_e32 v144, v124, v124
	v_mul_f32_e32 v145, v125, v125
	v_mul_f32_e32 v146, v126, v126
	v_mul_f32_e32 v147, v127, v127
	v_mul_f32_e32 v148, v120, v120
	v_mul_f32_e32 v149, v121, v121
	v_mul_f32_e32 v150, v122, v122
	v_mul_f32_e32 v151, v123, v123
	v_mul_f32_e32 v152, v116, v116
	v_mul_f32_e32 v153, v117, v117
	v_mul_f32_e32 v154, v118, v118
	v_mul_f32_e32 v155, v119, v119
	v_fma_f32 v140, v140, v158, v157
	v_fma_f32 v141, v141, v158, v157
	v_fma_f32 v142, v142, v158, v157
	v_fma_f32 v143, v143, v158, v157
	v_fma_f32 v144, v144, v158, v157
	v_fma_f32 v145, v145, v158, v157
	v_fma_f32 v146, v146, v158, v157
	v_fma_f32 v147, v147, v158, v157
	v_fma_f32 v148, v148, v158, v157
	v_fma_f32 v149, v149, v158, v157
	v_fma_f32 v150, v150, v158, v157
	v_fma_f32 v151, v151, v158, v157
	v_fma_f32 v152, v152, v158, v157
	v_fma_f32 v153, v153, v158, v157
	v_fma_f32 v154, v154, v158, v157
	v_fma_f32 v155, v155, v158, v157
	v_mul_f32_e32 v140, v128, v140
	v_mul_f32_e32 v141, v129, v141
	v_mul_f32_e32 v142, v130, v142
	v_mul_f32_e32 v143, v131, v143
	v_mul_f32_e32 v144, v124, v144
	v_mul_f32_e32 v145, v125, v145
	v_mul_f32_e32 v146, v126, v146
	v_mul_f32_e32 v147, v127, v147
	v_mul_f32_e32 v148, v120, v148
	v_mul_f32_e32 v149, v121, v149
	v_mul_f32_e32 v150, v122, v150
	v_mul_f32_e32 v151, v123, v151
	v_mul_f32_e32 v152, v116, v152
	v_mul_f32_e32 v153, v117, v153
	v_mul_f32_e32 v154, v118, v154
	v_mul_f32_e32 v155, v119, v155
	v_exp_f32_e32 v140, v140
	v_exp_f32_e32 v141, v141
	v_exp_f32_e32 v142, v142
	v_exp_f32_e32 v143, v143
	v_exp_f32_e32 v144, v144
	v_exp_f32_e32 v145, v145
	v_exp_f32_e32 v146, v146
	v_exp_f32_e32 v147, v147
	v_exp_f32_e32 v148, v148
	v_exp_f32_e32 v149, v149
	v_exp_f32_e32 v150, v150
	v_exp_f32_e32 v151, v151
	v_exp_f32_e32 v152, v152
	v_exp_f32_e32 v153, v153
	v_exp_f32_e32 v154, v154
	v_exp_f32_e32 v155, v155
	v_fma_f32 v140, v140, v159, v159
	v_fma_f32 v141, v141, v159, v159
	v_fma_f32 v142, v142, v159, v159
	v_fma_f32 v143, v143, v159, v159
	v_fma_f32 v144, v144, v159, v159
	v_fma_f32 v145, v145, v159, v159
	v_fma_f32 v146, v146, v159, v159
	v_fma_f32 v147, v147, v159, v159
	v_fma_f32 v148, v148, v159, v159
	v_fma_f32 v149, v149, v159, v159
	v_fma_f32 v150, v150, v159, v159
	v_fma_f32 v151, v151, v159, v159
	v_fma_f32 v152, v152, v159, v159
	v_fma_f32 v153, v153, v159, v159
	v_fma_f32 v154, v154, v159, v159
	v_fma_f32 v155, v155, v159, v159
	v_rcp_f32_e32 v140, v140
	v_rcp_f32_e32 v141, v141
	v_rcp_f32_e32 v142, v142
	v_rcp_f32_e32 v143, v143
	v_rcp_f32_e32 v144, v144
	v_rcp_f32_e32 v145, v145
	v_rcp_f32_e32 v146, v146
	v_rcp_f32_e32 v147, v147
	v_rcp_f32_e32 v148, v148
	v_rcp_f32_e32 v149, v149
	v_rcp_f32_e32 v150, v150
	v_rcp_f32_e32 v151, v151
	v_rcp_f32_e32 v152, v152
	v_rcp_f32_e32 v153, v153
	v_rcp_f32_e32 v154, v154
	v_rcp_f32_e32 v155, v155
	v_mul_f32_e32 v128, v128, v140
	v_mul_f32_e32 v129, v129, v141
	v_mul_f32_e32 v130, v130, v142
	v_mul_f32_e32 v131, v131, v143
	v_mul_f32_e32 v124, v124, v144
	v_mul_f32_e32 v125, v125, v145
	v_mul_f32_e32 v126, v126, v146
	v_mul_f32_e32 v127, v127, v147
	v_mul_f32_e32 v120, v120, v148
	v_mul_f32_e32 v121, v121, v149
	v_mul_f32_e32 v122, v122, v150
	v_mul_f32_e32 v123, v123, v151
	v_mul_f32_e32 v116, v116, v152
	v_mul_f32_e32 v117, v117, v153
	v_mul_f32_e32 v118, v118, v154
	v_mul_f32_e32 v119, v119, v155
	v_add_f32_e32 v162, v128, v129
	v_mul_f32_e32 v163, v128, v128
	v_fma_f32 v163, v129, v129, v163
	v_add_f32_e32 v162, v162, v130
	v_fma_f32 v163, v130, v130, v163
	v_add_f32_e32 v162, v162, v131
	v_fma_f32 v163, v131, v131, v163
	v_add_f32_e32 v162, v162, v124
	v_fma_f32 v163, v124, v124, v163
	v_add_f32_e32 v162, v162, v125
	v_fma_f32 v163, v125, v125, v163
	v_add_f32_e32 v162, v162, v126
	v_fma_f32 v163, v126, v126, v163
	v_add_f32_e32 v162, v162, v127
	v_fma_f32 v163, v127, v127, v163
	v_add_f32_e32 v162, v162, v120
	v_fma_f32 v163, v120, v120, v163
	v_add_f32_e32 v162, v162, v121
	v_fma_f32 v163, v121, v121, v163
	v_add_f32_e32 v162, v162, v122
	v_fma_f32 v163, v122, v122, v163
	v_add_f32_e32 v162, v162, v123
	v_fma_f32 v163, v123, v123, v163
	v_add_f32_e32 v162, v162, v116
	v_fma_f32 v163, v116, v116, v163
	v_add_f32_e32 v162, v162, v117
	v_fma_f32 v163, v117, v117, v163
	v_add_f32_e32 v162, v162, v118
	v_fma_f32 v163, v118, v118, v163
	v_add_f32_e32 v162, v162, v119
	v_fma_f32 v163, v119, v119, v163
	ds_swizzle_b32 v161, v162 offset:swizzle(SWAP,16)
	ds_swizzle_b32 v182, v163 offset:swizzle(SWAP,16)
	v_cvt_pk_bf16_f32 v128, v128, v129
	v_cvt_pk_bf16_f32 v129, v130, v131
	v_cvt_pk_bf16_f32 v130, v124, v125
	v_cvt_pk_bf16_f32 v131, v126, v127
	global_store_dwordx4 v[134:135], v[128:131], off
	v_cvt_pk_bf16_f32 v120, v120, v121
	v_cvt_pk_bf16_f32 v121, v122, v123
	v_cvt_pk_bf16_f32 v122, v116, v117
	v_cvt_pk_bf16_f32 v123, v118, v119
	global_store_dwordx4 v[134:135], v[120:123], off offset:256
	s_waitcnt lgkmcnt(0)
	v_add_f32_e32 v162, v162, v161
	v_add_f32_e32 v163, v163, v182
	v_mov_b32_e32 v183, v162
	v_mov_b32_e32 v184, v163
	s_mov_b64 s[0:1], 0x0
	v_lshl_add_u64 v[140:141], v[138:139], 0, s[0:1]
	v_permlane32_swap_b32_e32 v162, v183
	v_permlane32_swap_b32_e32 v163, v184
	s_mov_b64 s[8:9], exec
	s_and_b64 exec, exec, s[4:5]
	v_add_f32_e32 v162, v162, v183
	v_add_f32_e32 v163, v163, v184
	global_store_dwordx2 v[140:141], v[162:163], off
	s_mov_b64 exec, s[8:9]
	s_nop 1
	s_waitcnt lgkmcnt(0)
; __device__ __forceinline__ u32x4 pack8(const f32x4 a, const f32x4 b) { u32x4 w; w.x = cvt_pk_bf16(a[0], a[1]); w.y = cvt_pk_bf16(a[2], a[3]); w.z = cvt_pk_bf16(b[0], b[1]); w.w = cvt_pk_bf16(b[2], b[3]); return w; }
;     const float c0 = act == 1 ? -2.302208198f : -1.4426950408889634f, c1 = act == 1 ? -0.10294324f : 0.f;
; #pragma unroll
;     for (int ai = 0; ai < 2; ++ai) { if (ai == 1 && halfunit) break;
; #pragma unroll
;         for (int m = 0; m < 4; ++m) { bf16_t* rowp = base + (size_t)(row0 + ai * HALF + m * 16) * ldc + col0; float ls1 = 0.f, ls2 = 0.f; const float rf = rsr[ai * HALF + m * 16];
; #pragma unroll
;             for (int bj = 0; bj < 2; ++bj) { f32x4 v0 = acc[ai][bj][m][0] * rf, v1 = acc[ai][bj][m][1] * rf;
;                 if (act != 0) {
; #pragma unroll
;                     for (int e = 0; e < 4; ++e) { const float x0 = v0[e], x1 = v1[e];
;                         const float r0 = __builtin_amdgcn_rcpf(1.0f + __builtin_amdgcn_exp2f(x0 * (c0 + c1 * x0 * x0))), r1 = __builtin_amdgcn_rcpf(1.0f + __builtin_amdgcn_exp2f(x1 * (c0 + c1 * x1 * x1)));
;                         v0[e] = act == 1 ? x0 * r0 : r0; v1[e] = act == 1 ? x1 * r1 : r1; } }
;                 if (stat) {
; #pragma unroll
;                     for (int e = 0; e < 4; ++e) { ls1 += v0[e] + v1[e]; ls2 += v0[e] * v0[e] + v1[e] * v1[e]; } }
;                 *(u32x4*)(rowp + bj * HALF) = pack8(v0, v1); }
;             if (stat) { ls1 = xor_add<16>(ls1); ls1 = xor_add<32>(ls1); ls2 = xor_add<16>(ls2); ls2 = xor_add<32>(ls2);
;                 if (fq == 0) { f32x2 st2; st2.x = ls1; st2.y = ls2; *(f32x2*)(stat + (size_t)(row0 + ai * HALF + m * 16) * 16) = st2; } }
	v_mov_b32_e32 v156, v160
	ds_read_b32 v160, v205 offset:128
	v_mul_f32_e32 v158, v156, v156
	v_mul_f32_e32 v157, 0xc0135761, v156
	v_rcp_f32_e32 v159, v156
	v_mul_f32_e32 v158, v158, v156
	v_mul_f32_e32 v158, 0xbdd2d3e8, v158
	v_mul_f32_e32 v140, v112, v112
	v_mul_f32_e32 v141, v113, v113
	v_mul_f32_e32 v142, v114, v114
	v_mul_f32_e32 v143, v115, v115
	v_mul_f32_e32 v144, v108, v108
	v_mul_f32_e32 v145, v109, v109
	v_mul_f32_e32 v146, v110, v110
	v_mul_f32_e32 v147, v111, v111
	v_mul_f32_e32 v148, v104, v104
	v_mul_f32_e32 v149, v105, v105
	v_mul_f32_e32 v150, v106, v106
	v_mul_f32_e32 v151, v107, v107
	v_mul_f32_e32 v152, v100, v100
	v_mul_f32_e32 v153, v101, v101
	v_mul_f32_e32 v154, v102, v102
	v_mul_f32_e32 v155, v103, v103
	v_fma_f32 v140, v140, v158, v157
	v_fma_f32 v141, v141, v158, v157
	v_fma_f32 v142, v142, v158, v157
	v_fma_f32 v143, v143, v158, v157
	v_fma_f32 v144, v144, v158, v157
	v_fma_f32 v145, v145, v158, v157
	v_fma_f32 v146, v146, v158, v157
	v_fma_f32 v147, v147, v158, v157
	v_fma_f32 v148, v148, v158, v157
	v_fma_f32 v149, v149, v158, v157
	v_fma_f32 v150, v150, v158, v157
	v_fma_f32 v151, v151, v158, v157
	v_fma_f32 v152, v152, v158, v157
	v_fma_f32 v153, v153, v158, v157
	v_fma_f32 v154, v154, v158, v157
	v_fma_f32 v155, v155, v158, v157
	v_mul_f32_e32 v140, v112, v140
	v_mul_f32_e32 v141, v113, v141
	v_mul_f32_e32 v142, v114, v142
	v_mul_f32_e32 v143, v115, v143
	v_mul_f32_e32 v144, v108, v144
	v_mul_f32_e32 v145, v109, v145
	v_mul_f32_e32 v146, v110, v146
	v_mul_f32_e32 v147, v111, v147
	v_mul_f32_e32 v148, v104, v148
	v_mul_f32_e32 v149, v105, v149
	v_mul_f32_e32 v150, v106, v150
	v_mul_f32_e32 v151, v107, v151
	v_mul_f32_e32 v152, v100, v152
	v_mul_f32_e32 v153, v101, v153
	v_mul_f32_e32 v154, v102, v154
	v_mul_f32_e32 v155, v103, v155
	v_exp_f32_e32 v140, v140
	v_exp_f32_e32 v141, v141
	v_exp_f32_e32 v142, v142
	v_exp_f32_e32 v143, v143
	v_exp_f32_e32 v144, v144
	v_exp_f32_e32 v145, v145
	v_exp_f32_e32 v146, v146
	v_exp_f32_e32 v147, v147
	v_exp_f32_e32 v148, v148
	v_exp_f32_e32 v149, v149
	v_exp_f32_e32 v150, v150
	v_exp_f32_e32 v151, v151
	v_exp_f32_e32 v152, v152
	v_exp_f32_e32 v153, v153
	v_exp_f32_e32 v154, v154
	v_exp_f32_e32 v155, v155
	v_fma_f32 v140, v140, v159, v159
	v_fma_f32 v141, v141, v159, v159
	v_fma_f32 v142, v142, v159, v159
	v_fma_f32 v143, v143, v159, v159
	v_fma_f32 v144, v144, v159, v159
	v_fma_f32 v145, v145, v159, v159
	v_fma_f32 v146, v146, v159, v159
	v_fma_f32 v147, v147, v159, v159
	v_fma_f32 v148, v148, v159, v159
	v_fma_f32 v149, v149, v159, v159
	v_fma_f32 v150, v150, v159, v159
	v_fma_f32 v151, v151, v159, v159
	v_fma_f32 v152, v152, v159, v159
	v_fma_f32 v153, v153, v159, v159
	v_fma_f32 v154, v154, v159, v159
	v_fma_f32 v155, v155, v159, v159
	v_rcp_f32_e32 v140, v140
	v_rcp_f32_e32 v141, v141
	v_rcp_f32_e32 v142, v142
	v_rcp_f32_e32 v143, v143
	v_rcp_f32_e32 v144, v144
	v_rcp_f32_e32 v145, v145
	v_rcp_f32_e32 v146, v146
	v_rcp_f32_e32 v147, v147
	v_rcp_f32_e32 v148, v148
	v_rcp_f32_e32 v149, v149
	v_rcp_f32_e32 v150, v150
	v_rcp_f32_e32 v151, v151
	v_rcp_f32_e32 v152, v152
	v_rcp_f32_e32 v153, v153
	v_rcp_f32_e32 v154, v154
	v_rcp_f32_e32 v155, v155
	v_mul_f32_e32 v112, v112, v140
	v_mul_f32_e32 v113, v113, v141
	v_mul_f32_e32 v114, v114, v142
	v_mul_f32_e32 v115, v115, v143
	v_mul_f32_e32 v108, v108, v144
	v_mul_f32_e32 v109, v109, v145
	v_mul_f32_e32 v110, v110, v146
	v_mul_f32_e32 v111, v111, v147
	v_mul_f32_e32 v104, v104, v148
	v_mul_f32_e32 v105, v105, v149
	v_mul_f32_e32 v106, v106, v150
	v_mul_f32_e32 v107, v107, v151
	v_mul_f32_e32 v100, v100, v152
	v_mul_f32_e32 v101, v101, v153
	v_mul_f32_e32 v102, v102, v154
	v_mul_f32_e32 v103, v103, v155
	s_mov_b64 s[0:1], 0x4000
	v_lshl_add_u64 v[136:137], v[134:135], 0, s[0:1]
	v_add_f32_e32 v162, v112, v113
	v_mul_f32_e32 v163, v112, v112
	v_fma_f32 v163, v113, v113, v163
	v_add_f32_e32 v162, v162, v114
	v_fma_f32 v163, v114, v114, v163
	v_add_f32_e32 v162, v162, v115
	v_fma_f32 v163, v115, v115, v163
	v_add_f32_e32 v162, v162, v108
	v_fma_f32 v163, v108, v108, v163
	v_add_f32_e32 v162, v162, v109
	v_fma_f32 v163, v109, v109, v163
	v_add_f32_e32 v162, v162, v110
	v_fma_f32 v163, v110, v110, v163
	v_add_f32_e32 v162, v162, v111
	v_fma_f32 v163, v111, v111, v163
	v_add_f32_e32 v162, v162, v104
	v_fma_f32 v163, v104, v104, v163
	v_add_f32_e32 v162, v162, v105
	v_fma_f32 v163, v105, v105, v163
	v_add_f32_e32 v162, v162, v106
	v_fma_f32 v163, v106, v106, v163
	v_add_f32_e32 v162, v162, v107
	v_fma_f32 v163, v107, v107, v163
	v_add_f32_e32 v162, v162, v100
	v_fma_f32 v163, v100, v100, v163
	v_add_f32_e32 v162, v162, v101
	v_fma_f32 v163, v101, v101, v163
	v_add_f32_e32 v162, v162, v102
	v_fma_f32 v163, v102, v102, v163
	v_add_f32_e32 v162, v162, v103
	v_fma_f32 v163, v103, v103, v163
	ds_swizzle_b32 v161, v162 offset:swizzle(SWAP,16)
	ds_swizzle_b32 v182, v163 offset:swizzle(SWAP,16)
	v_cvt_pk_bf16_f32 v112, v112, v113
	v_cvt_pk_bf16_f32 v113, v114, v115
	v_cvt_pk_bf16_f32 v114, v108, v109
	v_cvt_pk_bf16_f32 v115, v110, v111
	global_store_dwordx4 v[136:137], v[112:115], off
	v_cvt_pk_bf16_f32 v104, v104, v105
	v_cvt_pk_bf16_f32 v105, v106, v107
	v_cvt_pk_bf16_f32 v106, v100, v101
	v_cvt_pk_bf16_f32 v107, v102, v103
	global_store_dwordx4 v[136:137], v[104:107], off offset:256
	s_waitcnt lgkmcnt(0)
	v_add_f32_e32 v162, v162, v161
	v_add_f32_e32 v163, v163, v182
	v_mov_b32_e32 v183, v162
	v_mov_b32_e32 v184, v163
	s_mov_b64 s[0:1], 0x400
	v_lshl_add_u64 v[140:141], v[138:139], 0, s[0:1]
	v_permlane32_swap_b32_e32 v162, v183
	v_permlane32_swap_b32_e32 v163, v184
	s_mov_b64 s[8:9], exec
	s_and_b64 exec, exec, s[4:5]
	v_add_f32_e32 v162, v162, v183
	v_add_f32_e32 v163, v163, v184
	global_store_dwordx2 v[140:141], v[162:163], off
	s_mov_b64 exec, s[8:9]
	s_nop 1
	s_waitcnt lgkmcnt(0)
; __device__ __forceinline__ u32x4 pack8(const f32x4 a, const f32x4 b) { u32x4 w; w.x = cvt_pk_bf16(a[0], a[1]); w.y = cvt_pk_bf16(a[2], a[3]); w.z = cvt_pk_bf16(b[0], b[1]); w.w = cvt_pk_bf16(b[2], b[3]); return w; }
;     const float c0 = act == 1 ? -2.302208198f : -1.4426950408889634f, c1 = act == 1 ? -0.10294324f : 0.f;
; #pragma unroll
;     for (int ai = 0; ai < 2; ++ai) { if (ai == 1 && halfunit) break;
; #pragma unroll
;         for (int m = 0; m < 4; ++m) { bf16_t* rowp = base + (size_t)(row0 + ai * HALF + m * 16) * ldc + col0; float ls1 = 0.f, ls2 = 0.f; const float rf = rsr[ai * HALF + m * 16];
; #pragma unroll
;             for (int bj = 0; bj < 2; ++bj) { f32x4 v0 = acc[ai][bj][m][0] * rf, v1 = acc[ai][bj][m][1] * rf;
;                 if (act != 0) {
; #pragma unroll
;                     for (int e = 0; e < 4; ++e) { const float x0 = v0[e], x1 = v1[e];
;                         const float r0 = __builtin_amdgcn_rcpf(1.0f + __builtin_amdgcn_exp2f(x0 * (c0 + c1 * x0 * x0))), r1 = __builtin_amdgcn_rcpf(1.0f + __builtin_amdgcn_exp2f(x1 * (c0 + c1 * x1 * x1)));
;                         v0[e] = act == 1 ? x0 * r0 : r0; v1[e] = act == 1 ? x1 * r1 : r1; } }
;                 if (stat) {
; #pragma unroll
;                     for (int e = 0; e < 4; ++e) { ls1 += v0[e] + v1[e]; ls2 += v0[e] * v0[e] + v1[e] * v1[e]; } }
;                 *(u32x4*)(rowp + bj * HALF) = pack8(v0, v1); }
;             if (stat) { ls1 = xor_add<16>(ls1); ls1 = xor_add<32>(ls1); ls2 = xor_add<16>(ls2); ls2 = xor_add<32>(ls2);
;                 if (fq == 0) { f32x2 st2; st2.x = ls1; st2.y = ls2; *(f32x2*)(stat + (size_t)(row0 + ai * HALF + m * 16) * 16) = st2; } }
	v_mov_b32_e32 v156, v160
	ds_read_b32 v160, v205 offset:192
	v_mul_f32_e32 v158, v156, v156
	v_mul_f32_e32 v157, 0xc0135761, v156
	v_rcp_f32_e32 v159, v156
	v_mul_f32_e32 v158, v158, v156
	v_mul_f32_e32 v158, 0xbdd2d3e8, v158
	v_mul_f32_e32 v140, v96, v96
	v_mul_f32_e32 v141, v97, v97
	v_mul_f32_e32 v142, v98, v98
	v_mul_f32_e32 v143, v99, v99
	v_mul_f32_e32 v144, v92, v92
	v_mul_f32_e32 v145, v93, v93
	v_mul_f32_e32 v146, v94, v94
	v_mul_f32_e32 v147, v95, v95
	v_mul_f32_e32 v148, v88, v88
	v_mul_f32_e32 v149, v89, v89
	v_mul_f32_e32 v150, v90, v90
	v_mul_f32_e32 v151, v91, v91
	v_mul_f32_e32 v152, v84, v84
	v_mul_f32_e32 v153, v85, v85
	v_mul_f32_e32 v154, v86, v86
	v_mul_f32_e32 v155, v87, v87
	v_fma_f32 v140, v140, v158, v157
	v_fma_f32 v141, v141, v158, v157
	v_fma_f32 v142, v142, v158, v157
	v_fma_f32 v143, v143, v158, v157
	v_fma_f32 v144, v144, v158, v157
	v_fma_f32 v145, v145, v158, v157
	v_fma_f32 v146, v146, v158, v157
	v_fma_f32 v147, v147, v158, v157
	v_fma_f32 v148, v148, v158, v157
	v_fma_f32 v149, v149, v158, v157
	v_fma_f32 v150, v150, v158, v157
	v_fma_f32 v151, v151, v158, v157
	v_fma_f32 v152, v152, v158, v157
	v_fma_f32 v153, v153, v158, v157
	v_fma_f32 v154, v154, v158, v157
	v_fma_f32 v155, v155, v158, v157
	v_mul_f32_e32 v140, v96, v140
	v_mul_f32_e32 v141, v97, v141
	v_mul_f32_e32 v142, v98, v142
	v_mul_f32_e32 v143, v99, v143
	v_mul_f32_e32 v144, v92, v144
	v_mul_f32_e32 v145, v93, v145
	v_mul_f32_e32 v146, v94, v146
	v_mul_f32_e32 v147, v95, v147
	v_mul_f32_e32 v148, v88, v148
	v_mul_f32_e32 v149, v89, v149
	v_mul_f32_e32 v150, v90, v150
	v_mul_f32_e32 v151, v91, v151
	v_mul_f32_e32 v152, v84, v152
	v_mul_f32_e32 v153, v85, v153
	v_mul_f32_e32 v154, v86, v154
	v_mul_f32_e32 v155, v87, v155
	v_exp_f32_e32 v140, v140
	v_exp_f32_e32 v141, v141
	v_exp_f32_e32 v142, v142
	v_exp_f32_e32 v143, v143
	v_exp_f32_e32 v144, v144
	v_exp_f32_e32 v145, v145
	v_exp_f32_e32 v146, v146
	v_exp_f32_e32 v147, v147
	v_exp_f32_e32 v148, v148
	v_exp_f32_e32 v149, v149
	v_exp_f32_e32 v150, v150
	v_exp_f32_e32 v151, v151
	v_exp_f32_e32 v152, v152
	v_exp_f32_e32 v153, v153
	v_exp_f32_e32 v154, v154
	v_exp_f32_e32 v155, v155
	v_fma_f32 v140, v140, v159, v159
	v_fma_f32 v141, v141, v159, v159
	v_fma_f32 v142, v142, v159, v159
	v_fma_f32 v143, v143, v159, v159
	v_fma_f32 v144, v144, v159, v159
	v_fma_f32 v145, v145, v159, v159
	v_fma_f32 v146, v146, v159, v159
	v_fma_f32 v147, v147, v159, v159
	v_fma_f32 v148, v148, v159, v159
	v_fma_f32 v149, v149, v159, v159
	v_fma_f32 v150, v150, v159, v159
	v_fma_f32 v151, v151, v159, v159
	v_fma_f32 v152, v152, v159, v159
	v_fma_f32 v153, v153, v159, v159
	v_fma_f32 v154, v154, v159, v159
	v_fma_f32 v155, v155, v159, v159
	v_rcp_f32_e32 v140, v140
	v_rcp_f32_e32 v141, v141
	v_rcp_f32_e32 v142, v142
	v_rcp_f32_e32 v143, v143
	v_rcp_f32_e32 v144, v144
	v_rcp_f32_e32 v145, v145
	v_rcp_f32_e32 v146, v146
	v_rcp_f32_e32 v147, v147
	v_rcp_f32_e32 v148, v148
	v_rcp_f32_e32 v149, v149
	v_rcp_f32_e32 v150, v150
	v_rcp_f32_e32 v151, v151
	v_rcp_f32_e32 v152, v152
	v_rcp_f32_e32 v153, v153
	v_rcp_f32_e32 v154, v154
	v_rcp_f32_e32 v155, v155
	v_mul_f32_e32 v96, v96, v140
	v_mul_f32_e32 v97, v97, v141
	v_mul_f32_e32 v98, v98, v142
	v_mul_f32_e32 v99, v99, v143
	v_mul_f32_e32 v92, v92, v144
	v_mul_f32_e32 v93, v93, v145
	v_mul_f32_e32 v94, v94, v146
	v_mul_f32_e32 v95, v95, v147
	v_mul_f32_e32 v88, v88, v148
	v_mul_f32_e32 v89, v89, v149
	v_mul_f32_e32 v90, v90, v150
	v_mul_f32_e32 v91, v91, v151
	v_mul_f32_e32 v84, v84, v152
	v_mul_f32_e32 v85, v85, v153
	v_mul_f32_e32 v86, v86, v154
	v_mul_f32_e32 v87, v87, v155
	s_mov_b64 s[0:1], 0x8000
	v_lshl_add_u64 v[136:137], v[134:135], 0, s[0:1]
	v_add_f32_e32 v162, v96, v97
	v_mul_f32_e32 v163, v96, v96
	v_fma_f32 v163, v97, v97, v163
	v_add_f32_e32 v162, v162, v98
	v_fma_f32 v163, v98, v98, v163
	v_add_f32_e32 v162, v162, v99
	v_fma_f32 v163, v99, v99, v163
	v_add_f32_e32 v162, v162, v92
	v_fma_f32 v163, v92, v92, v163
	v_add_f32_e32 v162, v162, v93
	v_fma_f32 v163, v93, v93, v163
	v_add_f32_e32 v162, v162, v94
	v_fma_f32 v163, v94, v94, v163
	v_add_f32_e32 v162, v162, v95
	v_fma_f32 v163, v95, v95, v163
	v_add_f32_e32 v162, v162, v88
	v_fma_f32 v163, v88, v88, v163
	v_add_f32_e32 v162, v162, v89
	v_fma_f32 v163, v89, v89, v163
	v_add_f32_e32 v162, v162, v90
	v_fma_f32 v163, v90, v90, v163
	v_add_f32_e32 v162, v162, v91
	v_fma_f32 v163, v91, v91, v163
	v_add_f32_e32 v162, v162, v84
	v_fma_f32 v163, v84, v84, v163
	v_add_f32_e32 v162, v162, v85
	v_fma_f32 v163, v85, v85, v163
	v_add_f32_e32 v162, v162, v86
	v_fma_f32 v163, v86, v86, v163
	v_add_f32_e32 v162, v162, v87
	v_fma_f32 v163, v87, v87, v163
	ds_swizzle_b32 v161, v162 offset:swizzle(SWAP,16)
	ds_swizzle_b32 v182, v163 offset:swizzle(SWAP,16)
	v_cvt_pk_bf16_f32 v96, v96, v97
	v_cvt_pk_bf16_f32 v97, v98, v99
	v_cvt_pk_bf16_f32 v98, v92, v93
	v_cvt_pk_bf16_f32 v99, v94, v95
	global_store_dwordx4 v[136:137], v[96:99], off
	v_cvt_pk_bf16_f32 v88, v88, v89
	v_cvt_pk_bf16_f32 v89, v90, v91
	v_cvt_pk_bf16_f32 v90, v84, v85
	v_cvt_pk_bf16_f32 v91, v86, v87
	global_store_dwordx4 v[136:137], v[88:91], off offset:256
	s_waitcnt lgkmcnt(0)
	v_add_f32_e32 v162, v162, v161
	v_add_f32_e32 v163, v163, v182
	v_mov_b32_e32 v183, v162
	v_mov_b32_e32 v184, v163
	s_mov_b64 s[0:1], 0x800
	v_lshl_add_u64 v[140:141], v[138:139], 0, s[0:1]
	v_permlane32_swap_b32_e32 v162, v183
	v_permlane32_swap_b32_e32 v163, v184
	s_mov_b64 s[8:9], exec
	s_and_b64 exec, exec, s[4:5]
	v_add_f32_e32 v162, v162, v183
	v_add_f32_e32 v163, v163, v184
	global_store_dwordx2 v[140:141], v[162:163], off
	s_mov_b64 exec, s[8:9]
	s_nop 1
	s_waitcnt lgkmcnt(0)
; __device__ __forceinline__ u32x4 pack8(const f32x4 a, const f32x4 b) { u32x4 w; w.x = cvt_pk_bf16(a[0], a[1]); w.y = cvt_pk_bf16(a[2], a[3]); w.z = cvt_pk_bf16(b[0], b[1]); w.w = cvt_pk_bf16(b[2], b[3]); return w; }
;     const float c0 = act == 1 ? -2.302208198f : -1.4426950408889634f, c1 = act == 1 ? -0.10294324f : 0.f;
; #pragma unroll
;     for (int ai = 0; ai < 2; ++ai) { if (ai == 1 && halfunit) break;
; #pragma unroll
;         for (int m = 0; m < 4; ++m) { bf16_t* rowp = base + (size_t)(row0 + ai * HALF + m * 16) * ldc + col0; float ls1 = 0.f, ls2 = 0.f; const float rf = rsr[ai * HALF + m * 16];
; #pragma unroll
;             for (int bj = 0; bj < 2; ++bj) { f32x4 v0 = acc[ai][bj][m][0] * rf, v1 = acc[ai][bj][m][1] * rf;
;                 if (act != 0) {
; #pragma unroll
;                     for (int e = 0; e < 4; ++e) { const float x0 = v0[e], x1 = v1[e];
;                         const float r0 = __builtin_amdgcn_rcpf(1.0f + __builtin_amdgcn_exp2f(x0 * (c0 + c1 * x0 * x0))), r1 = __builtin_amdgcn_rcpf(1.0f + __builtin_amdgcn_exp2f(x1 * (c0 + c1 * x1 * x1)));
;                         v0[e] = act == 1 ? x0 * r0 : r0; v1[e] = act == 1 ? x1 * r1 : r1; } }
;                 if (stat) {
; #pragma unroll
;                     for (int e = 0; e < 4; ++e) { ls1 += v0[e] + v1[e]; ls2 += v0[e] * v0[e] + v1[e] * v1[e]; } }
;                 *(u32x4*)(rowp + bj * HALF) = pack8(v0, v1); }
;             if (stat) { ls1 = xor_add<16>(ls1); ls1 = xor_add<32>(ls1); ls2 = xor_add<16>(ls2); ls2 = xor_add<32>(ls2);
;                 if (fq == 0) { f32x2 st2; st2.x = ls1; st2.y = ls2; *(f32x2*)(stat + (size_t)(row0 + ai * HALF + m * 16) * 16) = st2; } }
	v_mov_b32_e32 v156, v160
	ds_read_b32 v160, v205 offset:512
	v_mul_f32_e32 v158, v156, v156
	v_mul_f32_e32 v157, 0xc0135761, v156
	v_rcp_f32_e32 v159, v156
	v_mul_f32_e32 v158, v158, v156
	v_mul_f32_e32 v158, 0xbdd2d3e8, v158
	v_mul_f32_e32 v140, v80, v80
	v_mul_f32_e32 v141, v81, v81
	v_mul_f32_e32 v142, v82, v82
	v_mul_f32_e32 v143, v83, v83
	v_mul_f32_e32 v144, v76, v76
	v_mul_f32_e32 v145, v77, v77
	v_mul_f32_e32 v146, v78, v78
	v_mul_f32_e32 v147, v79, v79
	v_mul_f32_e32 v148, v72, v72
	v_mul_f32_e32 v149, v73, v73
	v_mul_f32_e32 v150, v74, v74
	v_mul_f32_e32 v151, v75, v75
	v_mul_f32_e32 v152, v68, v68
	v_mul_f32_e32 v153, v69, v69
	v_mul_f32_e32 v154, v70, v70
	v_mul_f32_e32 v155, v71, v71
	v_fma_f32 v140, v140, v158, v157
	v_fma_f32 v141, v141, v158, v157
	v_fma_f32 v142, v142, v158, v157
	v_fma_f32 v143, v143, v158, v157
	v_fma_f32 v144, v144, v158, v157
	v_fma_f32 v145, v145, v158, v157
	v_fma_f32 v146, v146, v158, v157
	v_fma_f32 v147, v147, v158, v157
	v_fma_f32 v148, v148, v158, v157
	v_fma_f32 v149, v149, v158, v157
	v_fma_f32 v150, v150, v158, v157
	v_fma_f32 v151, v151, v158, v157
	v_fma_f32 v152, v152, v158, v157
	v_fma_f32 v153, v153, v158, v157
	v_fma_f32 v154, v154, v158, v157
	v_fma_f32 v155, v155, v158, v157
	v_mul_f32_e32 v140, v80, v140
	v_mul_f32_e32 v141, v81, v141
	v_mul_f32_e32 v142, v82, v142
	v_mul_f32_e32 v143, v83, v143
	v_mul_f32_e32 v144, v76, v144
	v_mul_f32_e32 v145, v77, v145
	v_mul_f32_e32 v146, v78, v146
	v_mul_f32_e32 v147, v79, v147
	v_mul_f32_e32 v148, v72, v148
	v_mul_f32_e32 v149, v73, v149
	v_mul_f32_e32 v150, v74, v150
	v_mul_f32_e32 v151, v75, v151
	v_mul_f32_e32 v152, v68, v152
	v_mul_f32_e32 v153, v69, v153
	v_mul_f32_e32 v154, v70, v154
	v_mul_f32_e32 v155, v71, v155
	v_exp_f32_e32 v140, v140
	v_exp_f32_e32 v141, v141
	v_exp_f32_e32 v142, v142
	v_exp_f32_e32 v143, v143
	v_exp_f32_e32 v144, v144
	v_exp_f32_e32 v145, v145
	v_exp_f32_e32 v146, v146
	v_exp_f32_e32 v147, v147
	v_exp_f32_e32 v148, v148
	v_exp_f32_e32 v149, v149
	v_exp_f32_e32 v150, v150
	v_exp_f32_e32 v151, v151
	v_exp_f32_e32 v152, v152
	v_exp_f32_e32 v153, v153
	v_exp_f32_e32 v154, v154
	v_exp_f32_e32 v155, v155
	v_fma_f32 v140, v140, v159, v159
	v_fma_f32 v141, v141, v159, v159
	v_fma_f32 v142, v142, v159, v159
	v_fma_f32 v143, v143, v159, v159
	v_fma_f32 v144, v144, v159, v159
	v_fma_f32 v145, v145, v159, v159
	v_fma_f32 v146, v146, v159, v159
	v_fma_f32 v147, v147, v159, v159
	v_fma_f32 v148, v148, v159, v159
	v_fma_f32 v149, v149, v159, v159
	v_fma_f32 v150, v150, v159, v159
	v_fma_f32 v151, v151, v159, v159
	v_fma_f32 v152, v152, v159, v159
	v_fma_f32 v153, v153, v159, v159
	v_fma_f32 v154, v154, v159, v159
	v_fma_f32 v155, v155, v159, v159
	v_rcp_f32_e32 v140, v140
	v_rcp_f32_e32 v141, v141
	v_rcp_f32_e32 v142, v142
	v_rcp_f32_e32 v143, v143
	v_rcp_f32_e32 v144, v144
	v_rcp_f32_e32 v145, v145
	v_rcp_f32_e32 v146, v146
	v_rcp_f32_e32 v147, v147
	v_rcp_f32_e32 v148, v148
	v_rcp_f32_e32 v149, v149
	v_rcp_f32_e32 v150, v150
	v_rcp_f32_e32 v151, v151
	v_rcp_f32_e32 v152, v152
	v_rcp_f32_e32 v153, v153
	v_rcp_f32_e32 v154, v154
	v_rcp_f32_e32 v155, v155
	v_mul_f32_e32 v80, v80, v140
	v_mul_f32_e32 v81, v81, v141
	v_mul_f32_e32 v82, v82, v142
	v_mul_f32_e32 v83, v83, v143
	v_mul_f32_e32 v76, v76, v144
	v_mul_f32_e32 v77, v77, v145
	v_mul_f32_e32 v78, v78, v146
	v_mul_f32_e32 v79, v79, v147
	v_mul_f32_e32 v72, v72, v148
	v_mul_f32_e32 v73, v73, v149
	v_mul_f32_e32 v74, v74, v150
	v_mul_f32_e32 v75, v75, v151
	v_mul_f32_e32 v68, v68, v152
	v_mul_f32_e32 v69, v69, v153
	v_mul_f32_e32 v70, v70, v154
	v_mul_f32_e32 v71, v71, v155
	s_mov_b64 s[0:1], 0xc000
	v_lshl_add_u64 v[136:137], v[134:135], 0, s[0:1]
	v_add_f32_e32 v162, v80, v81
	v_mul_f32_e32 v163, v80, v80
	v_fma_f32 v163, v81, v81, v163
	v_add_f32_e32 v162, v162, v82
	v_fma_f32 v163, v82, v82, v163
	v_add_f32_e32 v162, v162, v83
	v_fma_f32 v163, v83, v83, v163
	v_add_f32_e32 v162, v162, v76
	v_fma_f32 v163, v76, v76, v163
	v_add_f32_e32 v162, v162, v77
	v_fma_f32 v163, v77, v77, v163
	v_add_f32_e32 v162, v162, v78
	v_fma_f32 v163, v78, v78, v163
	v_add_f32_e32 v162, v162, v79
	v_fma_f32 v163, v79, v79, v163
	v_add_f32_e32 v162, v162, v72
	v_fma_f32 v163, v72, v72, v163
	v_add_f32_e32 v162, v162, v73
	v_fma_f32 v163, v73, v73, v163
	v_add_f32_e32 v162, v162, v74
	v_fma_f32 v163, v74, v74, v163
	v_add_f32_e32 v162, v162, v75
	v_fma_f32 v163, v75, v75, v163
	v_add_f32_e32 v162, v162, v68
	v_fma_f32 v163, v68, v68, v163
	v_add_f32_e32 v162, v162, v69
	v_fma_f32 v163, v69, v69, v163
	v_add_f32_e32 v162, v162, v70
	v_fma_f32 v163, v70, v70, v163
	v_add_f32_e32 v162, v162, v71
	v_fma_f32 v163, v71, v71, v163
	ds_swizzle_b32 v161, v162 offset:swizzle(SWAP,16)
	ds_swizzle_b32 v182, v163 offset:swizzle(SWAP,16)
	v_cvt_pk_bf16_f32 v80, v80, v81
	v_cvt_pk_bf16_f32 v81, v82, v83
	v_cvt_pk_bf16_f32 v82, v76, v77
	v_cvt_pk_bf16_f32 v83, v78, v79
	global_store_dwordx4 v[136:137], v[80:83], off
	v_cvt_pk_bf16_f32 v72, v72, v73
	v_cvt_pk_bf16_f32 v73, v74, v75
	v_cvt_pk_bf16_f32 v74, v68, v69
	v_cvt_pk_bf16_f32 v75, v70, v71
	global_store_dwordx4 v[136:137], v[72:75], off offset:256
	s_waitcnt lgkmcnt(0)
	v_add_f32_e32 v162, v162, v161
	v_add_f32_e32 v163, v163, v182
	v_mov_b32_e32 v183, v162
	v_mov_b32_e32 v184, v163
	s_mov_b64 s[0:1], 0xc00
	v_lshl_add_u64 v[140:141], v[138:139], 0, s[0:1]
	v_permlane32_swap_b32_e32 v162, v183
	v_permlane32_swap_b32_e32 v163, v184
	s_mov_b64 s[8:9], exec
	s_and_b64 exec, exec, s[4:5]
	v_add_f32_e32 v162, v162, v183
	v_add_f32_e32 v163, v163, v184
	global_store_dwordx2 v[140:141], v[162:163], off
	s_mov_b64 exec, s[8:9]
	s_nop 1
	s_waitcnt lgkmcnt(0)
; __device__ __forceinline__ u32x4 pack8(const f32x4 a, const f32x4 b) { u32x4 w; w.x = cvt_pk_bf16(a[0], a[1]); w.y = cvt_pk_bf16(a[2], a[3]); w.z = cvt_pk_bf16(b[0], b[1]); w.w = cvt_pk_bf16(b[2], b[3]); return w; }
;     const float c0 = act == 1 ? -2.302208198f : -1.4426950408889634f, c1 = act == 1 ? -0.10294324f : 0.f;
; #pragma unroll
;     for (int ai = 0; ai < 2; ++ai) { if (ai == 1 && halfunit) break;
; #pragma unroll
;         for (int m = 0; m < 4; ++m) { bf16_t* rowp = base + (size_t)(row0 + ai * HALF + m * 16) * ldc + col0; float ls1 = 0.f, ls2 = 0.f; const float rf = rsr[ai * HALF + m * 16];
; #pragma unroll
;             for (int bj = 0; bj < 2; ++bj) { f32x4 v0 = acc[ai][bj][m][0] * rf, v1 = acc[ai][bj][m][1] * rf;
;                 if (act != 0) {
; #pragma unroll
;                     for (int e = 0; e < 4; ++e) { const float x0 = v0[e], x1 = v1[e];
;                         const float r0 = __builtin_amdgcn_rcpf(1.0f + __builtin_amdgcn_exp2f(x0 * (c0 + c1 * x0 * x0))), r1 = __builtin_amdgcn_rcpf(1.0f + __builtin_amdgcn_exp2f(x1 * (c0 + c1 * x1 * x1)));
;                         v0[e] = act == 1 ? x0 * r0 : r0; v1[e] = act == 1 ? x1 * r1 : r1; } }
;                 if (stat) {
; #pragma unroll
;                     for (int e = 0; e < 4; ++e) { ls1 += v0[e] + v1[e]; ls2 += v0[e] * v0[e] + v1[e] * v1[e]; } }
;                 *(u32x4*)(rowp + bj * HALF) = pack8(v0, v1); }
;             if (stat) { ls1 = xor_add<16>(ls1); ls1 = xor_add<32>(ls1); ls2 = xor_add<16>(ls2); ls2 = xor_add<32>(ls2);
;                 if (fq == 0) { f32x2 st2; st2.x = ls1; st2.y = ls2; *(f32x2*)(stat + (size_t)(row0 + ai * HALF + m * 16) * 16) = st2; } }
	v_mov_b32_e32 v156, v160
	ds_read_b32 v160, v205 offset:576
	v_mul_f32_e32 v158, v156, v156
	v_mul_f32_e32 v157, 0xc0135761, v156
	v_rcp_f32_e32 v159, v156
	v_mul_f32_e32 v158, v158, v156
	v_mul_f32_e32 v158, 0xbdd2d3e8, v158
	v_mul_f32_e32 v140, v64, v64
	v_mul_f32_e32 v141, v65, v65
	v_mul_f32_e32 v142, v66, v66
	v_mul_f32_e32 v143, v67, v67
	v_mul_f32_e32 v144, v60, v60
	v_mul_f32_e32 v145, v61, v61
	v_mul_f32_e32 v146, v62, v62
	v_mul_f32_e32 v147, v63, v63
	v_mul_f32_e32 v148, v56, v56
	v_mul_f32_e32 v149, v57, v57
	v_mul_f32_e32 v150, v58, v58
	v_mul_f32_e32 v151, v59, v59
	v_mul_f32_e32 v152, v52, v52
	v_mul_f32_e32 v153, v53, v53
	v_mul_f32_e32 v154, v54, v54
	v_mul_f32_e32 v155, v55, v55
	v_fma_f32 v140, v140, v158, v157
	v_fma_f32 v141, v141, v158, v157
	v_fma_f32 v142, v142, v158, v157
	v_fma_f32 v143, v143, v158, v157
	v_fma_f32 v144, v144, v158, v157
	v_fma_f32 v145, v145, v158, v157
	v_fma_f32 v146, v146, v158, v157
	v_fma_f32 v147, v147, v158, v157
	v_fma_f32 v148, v148, v158, v157
	v_fma_f32 v149, v149, v158, v157
	v_fma_f32 v150, v150, v158, v157
	v_fma_f32 v151, v151, v158, v157
	v_fma_f32 v152, v152, v158, v157
	v_fma_f32 v153, v153, v158, v157
	v_fma_f32 v154, v154, v158, v157
	v_fma_f32 v155, v155, v158, v157
	v_mul_f32_e32 v140, v64, v140
	v_mul_f32_e32 v141, v65, v141
	v_mul_f32_e32 v142, v66, v142
	v_mul_f32_e32 v143, v67, v143
	v_mul_f32_e32 v144, v60, v144
	v_mul_f32_e32 v145, v61, v145
	v_mul_f32_e32 v146, v62, v146
	v_mul_f32_e32 v147, v63, v147
	v_mul_f32_e32 v148, v56, v148
	v_mul_f32_e32 v149, v57, v149
	v_mul_f32_e32 v150, v58, v150
	v_mul_f32_e32 v151, v59, v151
	v_mul_f32_e32 v152, v52, v152
	v_mul_f32_e32 v153, v53, v153
	v_mul_f32_e32 v154, v54, v154
	v_mul_f32_e32 v155, v55, v155
	v_exp_f32_e32 v140, v140
	v_exp_f32_e32 v141, v141
	v_exp_f32_e32 v142, v142
	v_exp_f32_e32 v143, v143
	v_exp_f32_e32 v144, v144
	v_exp_f32_e32 v145, v145
	v_exp_f32_e32 v146, v146
	v_exp_f32_e32 v147, v147
	v_exp_f32_e32 v148, v148
	v_exp_f32_e32 v149, v149
	v_exp_f32_e32 v150, v150
	v_exp_f32_e32 v151, v151
	v_exp_f32_e32 v152, v152
	v_exp_f32_e32 v153, v153
	v_exp_f32_e32 v154, v154
	v_exp_f32_e32 v155, v155
	v_fma_f32 v140, v140, v159, v159
	v_fma_f32 v141, v141, v159, v159
	v_fma_f32 v142, v142, v159, v159
	v_fma_f32 v143, v143, v159, v159
	v_fma_f32 v144, v144, v159, v159
	v_fma_f32 v145, v145, v159, v159
	v_fma_f32 v146, v146, v159, v159
	v_fma_f32 v147, v147, v159, v159
	v_fma_f32 v148, v148, v159, v159
	v_fma_f32 v149, v149, v159, v159
	v_fma_f32 v150, v150, v159, v159
	v_fma_f32 v151, v151, v159, v159
	v_fma_f32 v152, v152, v159, v159
	v_fma_f32 v153, v153, v159, v159
	v_fma_f32 v154, v154, v159, v159
	v_fma_f32 v155, v155, v159, v159
	v_rcp_f32_e32 v140, v140
	v_rcp_f32_e32 v141, v141
	v_rcp_f32_e32 v142, v142
	v_rcp_f32_e32 v143, v143
	v_rcp_f32_e32 v144, v144
	v_rcp_f32_e32 v145, v145
	v_rcp_f32_e32 v146, v146
	v_rcp_f32_e32 v147, v147
	v_rcp_f32_e32 v148, v148
	v_rcp_f32_e32 v149, v149
	v_rcp_f32_e32 v150, v150
	v_rcp_f32_e32 v151, v151
	v_rcp_f32_e32 v152, v152
	v_rcp_f32_e32 v153, v153
	v_rcp_f32_e32 v154, v154
	v_rcp_f32_e32 v155, v155
	v_mul_f32_e32 v64, v64, v140
	v_mul_f32_e32 v65, v65, v141
	v_mul_f32_e32 v66, v66, v142
	v_mul_f32_e32 v67, v67, v143
	v_mul_f32_e32 v60, v60, v144
	v_mul_f32_e32 v61, v61, v145
	v_mul_f32_e32 v62, v62, v146
	v_mul_f32_e32 v63, v63, v147
	v_mul_f32_e32 v56, v56, v148
	v_mul_f32_e32 v57, v57, v149
	v_mul_f32_e32 v58, v58, v150
	v_mul_f32_e32 v59, v59, v151
	v_mul_f32_e32 v52, v52, v152
	v_mul_f32_e32 v53, v53, v153
	v_mul_f32_e32 v54, v54, v154
	v_mul_f32_e32 v55, v55, v155
	s_mov_b64 s[0:1], 0x20000
	v_lshl_add_u64 v[136:137], v[134:135], 0, s[0:1]
	v_add_f32_e32 v162, v64, v65
	v_mul_f32_e32 v163, v64, v64
	v_fma_f32 v163, v65, v65, v163
	v_add_f32_e32 v162, v162, v66
	v_fma_f32 v163, v66, v66, v163
	v_add_f32_e32 v162, v162, v67
	v_fma_f32 v163, v67, v67, v163
	v_add_f32_e32 v162, v162, v60
	v_fma_f32 v163, v60, v60, v163
	v_add_f32_e32 v162, v162, v61
	v_fma_f32 v163, v61, v61, v163
	v_add_f32_e32 v162, v162, v62
	v_fma_f32 v163, v62, v62, v163
	v_add_f32_e32 v162, v162, v63
	v_fma_f32 v163, v63, v63, v163
	v_add_f32_e32 v162, v162, v56
	v_fma_f32 v163, v56, v56, v163
	v_add_f32_e32 v162, v162, v57
	v_fma_f32 v163, v57, v57, v163
	v_add_f32_e32 v162, v162, v58
	v_fma_f32 v163, v58, v58, v163
	v_add_f32_e32 v162, v162, v59
	v_fma_f32 v163, v59, v59, v163
	v_add_f32_e32 v162, v162, v52
	v_fma_f32 v163, v52, v52, v163
	v_add_f32_e32 v162, v162, v53
	v_fma_f32 v163, v53, v53, v163
	v_add_f32_e32 v162, v162, v54
	v_fma_f32 v163, v54, v54, v163
	v_add_f32_e32 v162, v162, v55
	v_fma_f32 v163, v55, v55, v163
	ds_swizzle_b32 v161, v162 offset:swizzle(SWAP,16)
	ds_swizzle_b32 v182, v163 offset:swizzle(SWAP,16)
	v_cvt_pk_bf16_f32 v64, v64, v65
	v_cvt_pk_bf16_f32 v65, v66, v67
	v_cvt_pk_bf16_f32 v66, v60, v61
	v_cvt_pk_bf16_f32 v67, v62, v63
	global_store_dwordx4 v[136:137], v[64:67], off
	v_cvt_pk_bf16_f32 v56, v56, v57
	v_cvt_pk_bf16_f32 v57, v58, v59
	v_cvt_pk_bf16_f32 v58, v52, v53
	v_cvt_pk_bf16_f32 v59, v54, v55
	global_store_dwordx4 v[136:137], v[56:59], off offset:256
	s_waitcnt lgkmcnt(0)
	v_add_f32_e32 v162, v162, v161
	v_add_f32_e32 v163, v163, v182
	v_mov_b32_e32 v183, v162
	v_mov_b32_e32 v184, v163
	s_mov_b64 s[0:1], 0x2000
	v_lshl_add_u64 v[140:141], v[138:139], 0, s[0:1]
	v_permlane32_swap_b32_e32 v162, v183
	v_permlane32_swap_b32_e32 v163, v184
	s_mov_b64 s[8:9], exec
	s_and_b64 exec, exec, s[4:5]
	v_add_f32_e32 v162, v162, v183
	v_add_f32_e32 v163, v163, v184
	global_store_dwordx2 v[140:141], v[162:163], off
	s_mov_b64 exec, s[8:9]
	s_nop 1
	s_waitcnt lgkmcnt(0)
; __device__ __forceinline__ u32x4 pack8(const f32x4 a, const f32x4 b) { u32x4 w; w.x = cvt_pk_bf16(a[0], a[1]); w.y = cvt_pk_bf16(a[2], a[3]); w.z = cvt_pk_bf16(b[0], b[1]); w.w = cvt_pk_bf16(b[2], b[3]); return w; }
;     const float c0 = act == 1 ? -2.302208198f : -1.4426950408889634f, c1 = act == 1 ? -0.10294324f : 0.f;
; #pragma unroll
;     for (int ai = 0; ai < 2; ++ai) { if (ai == 1 && halfunit) break;
; #pragma unroll
;         for (int m = 0; m < 4; ++m) { bf16_t* rowp = base + (size_t)(row0 + ai * HALF + m * 16) * ldc + col0; float ls1 = 0.f, ls2 = 0.f; const float rf = rsr[ai * HALF + m * 16];
; #pragma unroll
;             for (int bj = 0; bj < 2; ++bj) { f32x4 v0 = acc[ai][bj][m][0] * rf, v1 = acc[ai][bj][m][1] * rf;
;                 if (act != 0) {
; #pragma unroll
;                     for (int e = 0; e < 4; ++e) { const float x0 = v0[e], x1 = v1[e];
;                         const float r0 = __builtin_amdgcn_rcpf(1.0f + __builtin_amdgcn_exp2f(x0 * (c0 + c1 * x0 * x0))), r1 = __builtin_amdgcn_rcpf(1.0f + __builtin_amdgcn_exp2f(x1 * (c0 + c1 * x1 * x1)));
;                         v0[e] = act == 1 ? x0 * r0 : r0; v1[e] = act == 1 ? x1 * r1 : r1; } }
;                 if (stat) {
; #pragma unroll
;                     for (int e = 0; e < 4; ++e) { ls1 += v0[e] + v1[e]; ls2 += v0[e] * v0[e] + v1[e] * v1[e]; } }
;                 *(u32x4*)(rowp + bj * HALF) = pack8(v0, v1); }
;             if (stat) { ls1 = xor_add<16>(ls1); ls1 = xor_add<32>(ls1); ls2 = xor_add<16>(ls2); ls2 = xor_add<32>(ls2);
;                 if (fq == 0) { f32x2 st2; st2.x = ls1; st2.y = ls2; *(f32x2*)(stat + (size_t)(row0 + ai * HALF + m * 16) * 16) = st2; } }
	v_mov_b32_e32 v156, v160
	ds_read_b32 v160, v205 offset:640
	v_mul_f32_e32 v158, v156, v156
	v_mul_f32_e32 v157, 0xc0135761, v156
	v_rcp_f32_e32 v159, v156
	v_mul_f32_e32 v158, v158, v156
	v_mul_f32_e32 v158, 0xbdd2d3e8, v158
	v_mul_f32_e32 v140, v48, v48
	v_mul_f32_e32 v141, v49, v49
	v_mul_f32_e32 v142, v50, v50
	v_mul_f32_e32 v143, v51, v51
	v_mul_f32_e32 v144, v44, v44
	v_mul_f32_e32 v145, v45, v45
	v_mul_f32_e32 v146, v46, v46
	v_mul_f32_e32 v147, v47, v47
	v_mul_f32_e32 v148, v40, v40
	v_mul_f32_e32 v149, v41, v41
	v_mul_f32_e32 v150, v42, v42
	v_mul_f32_e32 v151, v43, v43
	v_mul_f32_e32 v152, v36, v36
	v_mul_f32_e32 v153, v37, v37
	v_mul_f32_e32 v154, v38, v38
	v_mul_f32_e32 v155, v39, v39
	v_fma_f32 v140, v140, v158, v157
	v_fma_f32 v141, v141, v158, v157
	v_fma_f32 v142, v142, v158, v157
	v_fma_f32 v143, v143, v158, v157
	v_fma_f32 v144, v144, v158, v157
	v_fma_f32 v145, v145, v158, v157
	v_fma_f32 v146, v146, v158, v157
	v_fma_f32 v147, v147, v158, v157
	v_fma_f32 v148, v148, v158, v157
	v_fma_f32 v149, v149, v158, v157
	v_fma_f32 v150, v150, v158, v157
	v_fma_f32 v151, v151, v158, v157
	v_fma_f32 v152, v152, v158, v157
	v_fma_f32 v153, v153, v158, v157
	v_fma_f32 v154, v154, v158, v157
	v_fma_f32 v155, v155, v158, v157
	v_mul_f32_e32 v140, v48, v140
	v_mul_f32_e32 v141, v49, v141
	v_mul_f32_e32 v142, v50, v142
	v_mul_f32_e32 v143, v51, v143
	v_mul_f32_e32 v144, v44, v144
	v_mul_f32_e32 v145, v45, v145
	v_mul_f32_e32 v146, v46, v146
	v_mul_f32_e32 v147, v47, v147
	v_mul_f32_e32 v148, v40, v148
	v_mul_f32_e32 v149, v41, v149
	v_mul_f32_e32 v150, v42, v150
	v_mul_f32_e32 v151, v43, v151
	v_mul_f32_e32 v152, v36, v152
	v_mul_f32_e32 v153, v37, v153
	v_mul_f32_e32 v154, v38, v154
	v_mul_f32_e32 v155, v39, v155
	v_exp_f32_e32 v140, v140
	v_exp_f32_e32 v141, v141
	v_exp_f32_e32 v142, v142
	v_exp_f32_e32 v143, v143
	v_exp_f32_e32 v144, v144
	v_exp_f32_e32 v145, v145
	v_exp_f32_e32 v146, v146
	v_exp_f32_e32 v147, v147
	v_exp_f32_e32 v148, v148
	v_exp_f32_e32 v149, v149
	v_exp_f32_e32 v150, v150
	v_exp_f32_e32 v151, v151
	v_exp_f32_e32 v152, v152
	v_exp_f32_e32 v153, v153
	v_exp_f32_e32 v154, v154
	v_exp_f32_e32 v155, v155
	v_fma_f32 v140, v140, v159, v159
	v_fma_f32 v141, v141, v159, v159
	v_fma_f32 v142, v142, v159, v159
	v_fma_f32 v143, v143, v159, v159
	v_fma_f32 v144, v144, v159, v159
	v_fma_f32 v145, v145, v159, v159
	v_fma_f32 v146, v146, v159, v159
	v_fma_f32 v147, v147, v159, v159
	v_fma_f32 v148, v148, v159, v159
	v_fma_f32 v149, v149, v159, v159
	v_fma_f32 v150, v150, v159, v159
	v_fma_f32 v151, v151, v159, v159
	v_fma_f32 v152, v152, v159, v159
	v_fma_f32 v153, v153, v159, v159
	v_fma_f32 v154, v154, v159, v159
	v_fma_f32 v155, v155, v159, v159
	v_rcp_f32_e32 v140, v140
	v_rcp_f32_e32 v141, v141
	v_rcp_f32_e32 v142, v142
	v_rcp_f32_e32 v143, v143
	v_rcp_f32_e32 v144, v144
	v_rcp_f32_e32 v145, v145
	v_rcp_f32_e32 v146, v146
	v_rcp_f32_e32 v147, v147
	v_rcp_f32_e32 v148, v148
	v_rcp_f32_e32 v149, v149
	v_rcp_f32_e32 v150, v150
	v_rcp_f32_e32 v151, v151
	v_rcp_f32_e32 v152, v152
	v_rcp_f32_e32 v153, v153
	v_rcp_f32_e32 v154, v154
	v_rcp_f32_e32 v155, v155
	v_mul_f32_e32 v48, v48, v140
	v_mul_f32_e32 v49, v49, v141
	v_mul_f32_e32 v50, v50, v142
	v_mul_f32_e32 v51, v51, v143
	v_mul_f32_e32 v44, v44, v144
	v_mul_f32_e32 v45, v45, v145
	v_mul_f32_e32 v46, v46, v146
	v_mul_f32_e32 v47, v47, v147
	v_mul_f32_e32 v40, v40, v148
	v_mul_f32_e32 v41, v41, v149
	v_mul_f32_e32 v42, v42, v150
	v_mul_f32_e32 v43, v43, v151
	v_mul_f32_e32 v36, v36, v152
	v_mul_f32_e32 v37, v37, v153
	v_mul_f32_e32 v38, v38, v154
	v_mul_f32_e32 v39, v39, v155
	s_mov_b64 s[0:1], 0x24000
	v_lshl_add_u64 v[136:137], v[134:135], 0, s[0:1]
	v_add_f32_e32 v162, v48, v49
	v_mul_f32_e32 v163, v48, v48
	v_fma_f32 v163, v49, v49, v163
	v_add_f32_e32 v162, v162, v50
	v_fma_f32 v163, v50, v50, v163
	v_add_f32_e32 v162, v162, v51
	v_fma_f32 v163, v51, v51, v163
	v_add_f32_e32 v162, v162, v44
	v_fma_f32 v163, v44, v44, v163
	v_add_f32_e32 v162, v162, v45
	v_fma_f32 v163, v45, v45, v163
	v_add_f32_e32 v162, v162, v46
	v_fma_f32 v163, v46, v46, v163
	v_add_f32_e32 v162, v162, v47
	v_fma_f32 v163, v47, v47, v163
	v_add_f32_e32 v162, v162, v40
	v_fma_f32 v163, v40, v40, v163
	v_add_f32_e32 v162, v162, v41
	v_fma_f32 v163, v41, v41, v163
	v_add_f32_e32 v162, v162, v42
	v_fma_f32 v163, v42, v42, v163
	v_add_f32_e32 v162, v162, v43
	v_fma_f32 v163, v43, v43, v163
	v_add_f32_e32 v162, v162, v36
	v_fma_f32 v163, v36, v36, v163
	v_add_f32_e32 v162, v162, v37
	v_fma_f32 v163, v37, v37, v163
	v_add_f32_e32 v162, v162, v38
	v_fma_f32 v163, v38, v38, v163
	v_add_f32_e32 v162, v162, v39
	v_fma_f32 v163, v39, v39, v163
	ds_swizzle_b32 v161, v162 offset:swizzle(SWAP,16)
	ds_swizzle_b32 v182, v163 offset:swizzle(SWAP,16)
	v_cvt_pk_bf16_f32 v48, v48, v49
	v_cvt_pk_bf16_f32 v49, v50, v51
	v_cvt_pk_bf16_f32 v50, v44, v45
	v_cvt_pk_bf16_f32 v51, v46, v47
	global_store_dwordx4 v[136:137], v[48:51], off
	v_cvt_pk_bf16_f32 v40, v40, v41
	v_cvt_pk_bf16_f32 v41, v42, v43
	v_cvt_pk_bf16_f32 v42, v36, v37
	v_cvt_pk_bf16_f32 v43, v38, v39
	global_store_dwordx4 v[136:137], v[40:43], off offset:256
	s_waitcnt lgkmcnt(0)
	v_add_f32_e32 v162, v162, v161
	v_add_f32_e32 v163, v163, v182
	v_mov_b32_e32 v183, v162
	v_mov_b32_e32 v184, v163
	s_mov_b64 s[0:1], 0x2400
	v_lshl_add_u64 v[140:141], v[138:139], 0, s[0:1]
	v_permlane32_swap_b32_e32 v162, v183
	v_permlane32_swap_b32_e32 v163, v184
	s_mov_b64 s[8:9], exec
	s_and_b64 exec, exec, s[4:5]
	v_add_f32_e32 v162, v162, v183
	v_add_f32_e32 v163, v163, v184
	global_store_dwordx2 v[140:141], v[162:163], off
	s_mov_b64 exec, s[8:9]
	s_nop 1
	s_waitcnt lgkmcnt(0)
; __device__ __forceinline__ u32x4 pack8(const f32x4 a, const f32x4 b) { u32x4 w; w.x = cvt_pk_bf16(a[0], a[1]); w.y = cvt_pk_bf16(a[2], a[3]); w.z = cvt_pk_bf16(b[0], b[1]); w.w = cvt_pk_bf16(b[2], b[3]); return w; }
;     const float c0 = act == 1 ? -2.302208198f : -1.4426950408889634f, c1 = act == 1 ? -0.10294324f : 0.f;
; #pragma unroll
;     for (int ai = 0; ai < 2; ++ai) { if (ai == 1 && halfunit) break;
; #pragma unroll
;         for (int m = 0; m < 4; ++m) { bf16_t* rowp = base + (size_t)(row0 + ai * HALF + m * 16) * ldc + col0; float ls1 = 0.f, ls2 = 0.f; const float rf = rsr[ai * HALF + m * 16];
; #pragma unroll
;             for (int bj = 0; bj < 2; ++bj) { f32x4 v0 = acc[ai][bj][m][0] * rf, v1 = acc[ai][bj][m][1] * rf;
;                 if (act != 0) {
; #pragma unroll
;                     for (int e = 0; e < 4; ++e) { const float x0 = v0[e], x1 = v1[e];
;                         const float r0 = __builtin_amdgcn_rcpf(1.0f + __builtin_amdgcn_exp2f(x0 * (c0 + c1 * x0 * x0))), r1 = __builtin_amdgcn_rcpf(1.0f + __builtin_amdgcn_exp2f(x1 * (c0 + c1 * x1 * x1)));
;                         v0[e] = act == 1 ? x0 * r0 : r0; v1[e] = act == 1 ? x1 * r1 : r1; } }
;                 if (stat) {
; #pragma unroll
;                     for (int e = 0; e < 4; ++e) { ls1 += v0[e] + v1[e]; ls2 += v0[e] * v0[e] + v1[e] * v1[e]; } }
;                 *(u32x4*)(rowp + bj * HALF) = pack8(v0, v1); }
;             if (stat) { ls1 = xor_add<16>(ls1); ls1 = xor_add<32>(ls1); ls2 = xor_add<16>(ls2); ls2 = xor_add<32>(ls2);
;                 if (fq == 0) { f32x2 st2; st2.x = ls1; st2.y = ls2; *(f32x2*)(stat + (size_t)(row0 + ai * HALF + m * 16) * 16) = st2; } }
	v_mov_b32_e32 v156, v160
	ds_read_b32 v160, v205 offset:704
	v_mul_f32_e32 v158, v156, v156
	v_mul_f32_e32 v157, 0xc0135761, v156
	v_rcp_f32_e32 v159, v156
	v_mul_f32_e32 v158, v158, v156
	v_mul_f32_e32 v158, 0xbdd2d3e8, v158
	v_mul_f32_e32 v140, v32, v32
	v_mul_f32_e32 v141, v33, v33
	v_mul_f32_e32 v142, v34, v34
	v_mul_f32_e32 v143, v35, v35
	v_mul_f32_e32 v144, v28, v28
	v_mul_f32_e32 v145, v29, v29
	v_mul_f32_e32 v146, v30, v30
	v_mul_f32_e32 v147, v31, v31
	v_mul_f32_e32 v148, v24, v24
	v_mul_f32_e32 v149, v25, v25
	v_mul_f32_e32 v150, v26, v26
	v_mul_f32_e32 v151, v27, v27
	v_mul_f32_e32 v152, v20, v20
	v_mul_f32_e32 v153, v21, v21
	v_mul_f32_e32 v154, v22, v22
	v_mul_f32_e32 v155, v23, v23
	v_fma_f32 v140, v140, v158, v157
	v_fma_f32 v141, v141, v158, v157
	v_fma_f32 v142, v142, v158, v157
	v_fma_f32 v143, v143, v158, v157
	v_fma_f32 v144, v144, v158, v157
	v_fma_f32 v145, v145, v158, v157
	v_fma_f32 v146, v146, v158, v157
	v_fma_f32 v147, v147, v158, v157
	v_fma_f32 v148, v148, v158, v157
	v_fma_f32 v149, v149, v158, v157
	v_fma_f32 v150, v150, v158, v157
	v_fma_f32 v151, v151, v158, v157
	v_fma_f32 v152, v152, v158, v157
	v_fma_f32 v153, v153, v158, v157
	v_fma_f32 v154, v154, v158, v157
	v_fma_f32 v155, v155, v158, v157
	v_mul_f32_e32 v140, v32, v140
	v_mul_f32_e32 v141, v33, v141
	v_mul_f32_e32 v142, v34, v142
	v_mul_f32_e32 v143, v35, v143
	v_mul_f32_e32 v144, v28, v144
	v_mul_f32_e32 v145, v29, v145
	v_mul_f32_e32 v146, v30, v146
	v_mul_f32_e32 v147, v31, v147
	v_mul_f32_e32 v148, v24, v148
	v_mul_f32_e32 v149, v25, v149
	v_mul_f32_e32 v150, v26, v150
	v_mul_f32_e32 v151, v27, v151
	v_mul_f32_e32 v152, v20, v152
	v_mul_f32_e32 v153, v21, v153
	v_mul_f32_e32 v154, v22, v154
	v_mul_f32_e32 v155, v23, v155
	v_exp_f32_e32 v140, v140
	v_exp_f32_e32 v141, v141
	v_exp_f32_e32 v142, v142
	v_exp_f32_e32 v143, v143
	v_exp_f32_e32 v144, v144
	v_exp_f32_e32 v145, v145
	v_exp_f32_e32 v146, v146
	v_exp_f32_e32 v147, v147
	v_exp_f32_e32 v148, v148
	v_exp_f32_e32 v149, v149
	v_exp_f32_e32 v150, v150
	v_exp_f32_e32 v151, v151
	v_exp_f32_e32 v152, v152
	v_exp_f32_e32 v153, v153
	v_exp_f32_e32 v154, v154
	v_exp_f32_e32 v155, v155
	v_fma_f32 v140, v140, v159, v159
	v_fma_f32 v141, v141, v159, v159
	v_fma_f32 v142, v142, v159, v159
	v_fma_f32 v143, v143, v159, v159
	v_fma_f32 v144, v144, v159, v159
	v_fma_f32 v145, v145, v159, v159
	v_fma_f32 v146, v146, v159, v159
	v_fma_f32 v147, v147, v159, v159
	v_fma_f32 v148, v148, v159, v159
	v_fma_f32 v149, v149, v159, v159
	v_fma_f32 v150, v150, v159, v159
	v_fma_f32 v151, v151, v159, v159
	v_fma_f32 v152, v152, v159, v159
	v_fma_f32 v153, v153, v159, v159
	v_fma_f32 v154, v154, v159, v159
	v_fma_f32 v155, v155, v159, v159
	v_rcp_f32_e32 v140, v140
	v_rcp_f32_e32 v141, v141
	v_rcp_f32_e32 v142, v142
	v_rcp_f32_e32 v143, v143
	v_rcp_f32_e32 v144, v144
	v_rcp_f32_e32 v145, v145
	v_rcp_f32_e32 v146, v146
	v_rcp_f32_e32 v147, v147
	v_rcp_f32_e32 v148, v148
	v_rcp_f32_e32 v149, v149
	v_rcp_f32_e32 v150, v150
	v_rcp_f32_e32 v151, v151
	v_rcp_f32_e32 v152, v152
	v_rcp_f32_e32 v153, v153
	v_rcp_f32_e32 v154, v154
	v_rcp_f32_e32 v155, v155
	v_mul_f32_e32 v32, v32, v140
	v_mul_f32_e32 v33, v33, v141
	v_mul_f32_e32 v34, v34, v142
	v_mul_f32_e32 v35, v35, v143
	v_mul_f32_e32 v28, v28, v144
	v_mul_f32_e32 v29, v29, v145
	v_mul_f32_e32 v30, v30, v146
	v_mul_f32_e32 v31, v31, v147
	v_mul_f32_e32 v24, v24, v148
	v_mul_f32_e32 v25, v25, v149
	v_mul_f32_e32 v26, v26, v150
	v_mul_f32_e32 v27, v27, v151
	v_mul_f32_e32 v20, v20, v152
	v_mul_f32_e32 v21, v21, v153
	v_mul_f32_e32 v22, v22, v154
	v_mul_f32_e32 v23, v23, v155
	s_mov_b64 s[0:1], 0x28000
	v_lshl_add_u64 v[136:137], v[134:135], 0, s[0:1]
	v_add_f32_e32 v162, v32, v33
	v_mul_f32_e32 v163, v32, v32
	v_fma_f32 v163, v33, v33, v163
	v_add_f32_e32 v162, v162, v34
	v_fma_f32 v163, v34, v34, v163
	v_add_f32_e32 v162, v162, v35
	v_fma_f32 v163, v35, v35, v163
	v_add_f32_e32 v162, v162, v28
	v_fma_f32 v163, v28, v28, v163
	v_add_f32_e32 v162, v162, v29
	v_fma_f32 v163, v29, v29, v163
	v_add_f32_e32 v162, v162, v30
	v_fma_f32 v163, v30, v30, v163
	v_add_f32_e32 v162, v162, v31
	v_fma_f32 v163, v31, v31, v163
	v_add_f32_e32 v162, v162, v24
	v_fma_f32 v163, v24, v24, v163
	v_add_f32_e32 v162, v162, v25
	v_fma_f32 v163, v25, v25, v163
	v_add_f32_e32 v162, v162, v26
	v_fma_f32 v163, v26, v26, v163
	v_add_f32_e32 v162, v162, v27
	v_fma_f32 v163, v27, v27, v163
	v_add_f32_e32 v162, v162, v20
	v_fma_f32 v163, v20, v20, v163
	v_add_f32_e32 v162, v162, v21
	v_fma_f32 v163, v21, v21, v163
	v_add_f32_e32 v162, v162, v22
	v_fma_f32 v163, v22, v22, v163
	v_add_f32_e32 v162, v162, v23
	v_fma_f32 v163, v23, v23, v163
	ds_swizzle_b32 v161, v162 offset:swizzle(SWAP,16)
	ds_swizzle_b32 v182, v163 offset:swizzle(SWAP,16)
	v_cvt_pk_bf16_f32 v32, v32, v33
	v_cvt_pk_bf16_f32 v33, v34, v35
	v_cvt_pk_bf16_f32 v34, v28, v29
	v_cvt_pk_bf16_f32 v35, v30, v31
	global_store_dwordx4 v[136:137], v[32:35], off
	v_cvt_pk_bf16_f32 v24, v24, v25
	v_cvt_pk_bf16_f32 v25, v26, v27
	v_cvt_pk_bf16_f32 v26, v20, v21
	v_cvt_pk_bf16_f32 v27, v22, v23
	global_store_dwordx4 v[136:137], v[24:27], off offset:256
	s_waitcnt lgkmcnt(0)
	v_add_f32_e32 v162, v162, v161
	v_add_f32_e32 v163, v163, v182
	v_mov_b32_e32 v183, v162
	v_mov_b32_e32 v184, v163
	s_mov_b64 s[0:1], 0x2800
	v_lshl_add_u64 v[140:141], v[138:139], 0, s[0:1]
	v_permlane32_swap_b32_e32 v162, v183
	v_permlane32_swap_b32_e32 v163, v184
	s_mov_b64 s[8:9], exec
	s_and_b64 exec, exec, s[4:5]
	v_add_f32_e32 v162, v162, v183
	v_add_f32_e32 v163, v163, v184
	global_store_dwordx2 v[140:141], v[162:163], off
	s_mov_b64 exec, s[8:9]
	s_nop 1
	s_waitcnt lgkmcnt(0)
; __device__ __forceinline__ u32x4 pack8(const f32x4 a, const f32x4 b) { u32x4 w; w.x = cvt_pk_bf16(a[0], a[1]); w.y = cvt_pk_bf16(a[2], a[3]); w.z = cvt_pk_bf16(b[0], b[1]); w.w = cvt_pk_bf16(b[2], b[3]); return w; }
;     const float c0 = act == 1 ? -2.302208198f : -1.4426950408889634f, c1 = act == 1 ? -0.10294324f : 0.f;
; #pragma unroll
;     for (int ai = 0; ai < 2; ++ai) { if (ai == 1 && halfunit) break;
; #pragma unroll
;         for (int m = 0; m < 4; ++m) { bf16_t* rowp = base + (size_t)(row0 + ai * HALF + m * 16) * ldc + col0; float ls1 = 0.f, ls2 = 0.f; const float rf = rsr[ai * HALF + m * 16];
; #pragma unroll
;             for (int bj = 0; bj < 2; ++bj) { f32x4 v0 = acc[ai][bj][m][0] * rf, v1 = acc[ai][bj][m][1] * rf;
;                 if (act != 0) {
; #pragma unroll
;                     for (int e = 0; e < 4; ++e) { const float x0 = v0[e], x1 = v1[e];
;                         const float r0 = __builtin_amdgcn_rcpf(1.0f + __builtin_amdgcn_exp2f(x0 * (c0 + c1 * x0 * x0))), r1 = __builtin_amdgcn_rcpf(1.0f + __builtin_amdgcn_exp2f(x1 * (c0 + c1 * x1 * x1)));
;                         v0[e] = act == 1 ? x0 * r0 : r0; v1[e] = act == 1 ? x1 * r1 : r1; } }
;                 if (stat) {
; #pragma unroll
;                     for (int e = 0; e < 4; ++e) { ls1 += v0[e] + v1[e]; ls2 += v0[e] * v0[e] + v1[e] * v1[e]; } }
;                 *(u32x4*)(rowp + bj * HALF) = pack8(v0, v1); }
;             if (stat) { ls1 = xor_add<16>(ls1); ls1 = xor_add<32>(ls1); ls2 = xor_add<16>(ls2); ls2 = xor_add<32>(ls2);
;                 if (fq == 0) { f32x2 st2; st2.x = ls1; st2.y = ls2; *(f32x2*)(stat + (size_t)(row0 + ai * HALF + m * 16) * 16) = st2; } }
	v_mov_b32_e32 v156, v160
	v_mul_f32_e32 v158, v156, v156
	v_mul_f32_e32 v157, 0xc0135761, v156
	v_rcp_f32_e32 v159, v156
	v_mul_f32_e32 v158, v158, v156
	v_mul_f32_e32 v158, 0xbdd2d3e8, v158
	v_mul_f32_e32 v140, v16, v16
	v_mul_f32_e32 v141, v17, v17
	v_mul_f32_e32 v142, v18, v18
	v_mul_f32_e32 v143, v19, v19
	v_mul_f32_e32 v144, v12, v12
	v_mul_f32_e32 v145, v13, v13
	v_mul_f32_e32 v146, v14, v14
	v_mul_f32_e32 v147, v15, v15
	v_mul_f32_e32 v148, v8, v8
	v_mul_f32_e32 v149, v9, v9
	v_mul_f32_e32 v150, v10, v10
	v_mul_f32_e32 v151, v11, v11
	v_mul_f32_e32 v152, v4, v4
	v_mul_f32_e32 v153, v5, v5
	v_mul_f32_e32 v154, v6, v6
	v_mul_f32_e32 v155, v7, v7
	v_fma_f32 v140, v140, v158, v157
	v_fma_f32 v141, v141, v158, v157
	v_fma_f32 v142, v142, v158, v157
	v_fma_f32 v143, v143, v158, v157
	v_fma_f32 v144, v144, v158, v157
	v_fma_f32 v145, v145, v158, v157
	v_fma_f32 v146, v146, v158, v157
	v_fma_f32 v147, v147, v158, v157
	v_fma_f32 v148, v148, v158, v157
	v_fma_f32 v149, v149, v158, v157
	v_fma_f32 v150, v150, v158, v157
	v_fma_f32 v151, v151, v158, v157
	v_fma_f32 v152, v152, v158, v157
	v_fma_f32 v153, v153, v158, v157
	v_fma_f32 v154, v154, v158, v157
	v_fma_f32 v155, v155, v158, v157
	v_mul_f32_e32 v140, v16, v140
	v_mul_f32_e32 v141, v17, v141
	v_mul_f32_e32 v142, v18, v142
	v_mul_f32_e32 v143, v19, v143
	v_mul_f32_e32 v144, v12, v144
	v_mul_f32_e32 v145, v13, v145
	v_mul_f32_e32 v146, v14, v146
	v_mul_f32_e32 v147, v15, v147
	v_mul_f32_e32 v148, v8, v148
	v_mul_f32_e32 v149, v9, v149
	v_mul_f32_e32 v150, v10, v150
	v_mul_f32_e32 v151, v11, v151
	v_mul_f32_e32 v152, v4, v152
	v_mul_f32_e32 v153, v5, v153
	v_mul_f32_e32 v154, v6, v154
	v_mul_f32_e32 v155, v7, v155
	v_exp_f32_e32 v140, v140
	v_exp_f32_e32 v141, v141
	v_exp_f32_e32 v142, v142
	v_exp_f32_e32 v143, v143
	v_exp_f32_e32 v144, v144
	v_exp_f32_e32 v145, v145
	v_exp_f32_e32 v146, v146
	v_exp_f32_e32 v147, v147
	v_exp_f32_e32 v148, v148
	v_exp_f32_e32 v149, v149
	v_exp_f32_e32 v150, v150
	v_exp_f32_e32 v151, v151
	v_exp_f32_e32 v152, v152
	v_exp_f32_e32 v153, v153
	v_exp_f32_e32 v154, v154
	v_exp_f32_e32 v155, v155
	v_fma_f32 v140, v140, v159, v159
	v_fma_f32 v141, v141, v159, v159
	v_fma_f32 v142, v142, v159, v159
	v_fma_f32 v143, v143, v159, v159
	v_fma_f32 v144, v144, v159, v159
	v_fma_f32 v145, v145, v159, v159
	v_fma_f32 v146, v146, v159, v159
	v_fma_f32 v147, v147, v159, v159
	v_fma_f32 v148, v148, v159, v159
	v_fma_f32 v149, v149, v159, v159
	v_fma_f32 v150, v150, v159, v159
	v_fma_f32 v151, v151, v159, v159
	v_fma_f32 v152, v152, v159, v159
	v_fma_f32 v153, v153, v159, v159
	v_fma_f32 v154, v154, v159, v159
	v_fma_f32 v155, v155, v159, v159
	v_rcp_f32_e32 v140, v140
	v_rcp_f32_e32 v141, v141
	v_rcp_f32_e32 v142, v142
	v_rcp_f32_e32 v143, v143
	v_rcp_f32_e32 v144, v144
	v_rcp_f32_e32 v145, v145
	v_rcp_f32_e32 v146, v146
	v_rcp_f32_e32 v147, v147
	v_rcp_f32_e32 v148, v148
	v_rcp_f32_e32 v149, v149
	v_rcp_f32_e32 v150, v150
	v_rcp_f32_e32 v151, v151
	v_rcp_f32_e32 v152, v152
	v_rcp_f32_e32 v153, v153
	v_rcp_f32_e32 v154, v154
	v_rcp_f32_e32 v155, v155
	v_mul_f32_e32 v16, v16, v140
	v_mul_f32_e32 v17, v17, v141
	v_mul_f32_e32 v18, v18, v142
	v_mul_f32_e32 v19, v19, v143
	v_mul_f32_e32 v12, v12, v144
	v_mul_f32_e32 v13, v13, v145
	v_mul_f32_e32 v14, v14, v146
	v_mul_f32_e32 v15, v15, v147
	v_mul_f32_e32 v8, v8, v148
	v_mul_f32_e32 v9, v9, v149
	v_mul_f32_e32 v10, v10, v150
	v_mul_f32_e32 v11, v11, v151
	v_mul_f32_e32 v4, v4, v152
	v_mul_f32_e32 v5, v5, v153
	v_mul_f32_e32 v6, v6, v154
	v_mul_f32_e32 v7, v7, v155
	s_mov_b64 s[0:1], 0x2c000
	v_lshl_add_u64 v[136:137], v[134:135], 0, s[0:1]
	v_add_f32_e32 v162, v16, v17
	v_mul_f32_e32 v163, v16, v16
	v_fma_f32 v163, v17, v17, v163
	v_add_f32_e32 v162, v162, v18
	v_fma_f32 v163, v18, v18, v163
	v_add_f32_e32 v162, v162, v19
	v_fma_f32 v163, v19, v19, v163
	v_add_f32_e32 v162, v162, v12
	v_fma_f32 v163, v12, v12, v163
	v_add_f32_e32 v162, v162, v13
	v_fma_f32 v163, v13, v13, v163
	v_add_f32_e32 v162, v162, v14
	v_fma_f32 v163, v14, v14, v163
	v_add_f32_e32 v162, v162, v15
	v_fma_f32 v163, v15, v15, v163
	v_add_f32_e32 v162, v162, v8
	v_fma_f32 v163, v8, v8, v163
	v_add_f32_e32 v162, v162, v9
	v_fma_f32 v163, v9, v9, v163
	v_add_f32_e32 v162, v162, v10
	v_fma_f32 v163, v10, v10, v163
	v_add_f32_e32 v162, v162, v11
	v_fma_f32 v163, v11, v11, v163
	v_add_f32_e32 v162, v162, v4
	v_fma_f32 v163, v4, v4, v163
	v_add_f32_e32 v162, v162, v5
	v_fma_f32 v163, v5, v5, v163
	v_add_f32_e32 v162, v162, v6
	v_fma_f32 v163, v6, v6, v163
	v_add_f32_e32 v162, v162, v7
	v_fma_f32 v163, v7, v7, v163
	ds_swizzle_b32 v161, v162 offset:swizzle(SWAP,16)
	ds_swizzle_b32 v182, v163 offset:swizzle(SWAP,16)
	v_cvt_pk_bf16_f32 v16, v16, v17
	v_cvt_pk_bf16_f32 v17, v18, v19
	v_cvt_pk_bf16_f32 v18, v12, v13
	v_cvt_pk_bf16_f32 v19, v14, v15
	global_store_dwordx4 v[136:137], v[16:19], off
	v_cvt_pk_bf16_f32 v8, v8, v9
	v_cvt_pk_bf16_f32 v9, v10, v11
	v_cvt_pk_bf16_f32 v10, v4, v5
	v_cvt_pk_bf16_f32 v11, v6, v7
	global_store_dwordx4 v[136:137], v[8:11], off offset:256
	s_waitcnt lgkmcnt(0)
	v_add_f32_e32 v162, v162, v161
	v_add_f32_e32 v163, v163, v182
	v_mov_b32_e32 v183, v162
	v_mov_b32_e32 v184, v163
	s_mov_b64 s[0:1], 0x2c00
	v_lshl_add_u64 v[140:141], v[138:139], 0, s[0:1]
	v_permlane32_swap_b32_e32 v162, v183
	v_permlane32_swap_b32_e32 v163, v184
	s_mov_b64 s[8:9], exec
	s_and_b64 exec, exec, s[4:5]
	v_add_f32_e32 v162, v162, v183
	v_add_f32_e32 v163, v163, v184
	global_store_dwordx2 v[140:141], v[162:163], off
	s_mov_b64 exec, s[8:9]
	s_nop 1
	s_branch .Lt8_end

; #define PG8_WAIT_V(n) asm volatile("s_waitcnt vmcnt(" #n ")" ::: "memory")
; #define PG8_BAR __builtin_amdgcn_s_barrier()
; template <class Epi, class Sched, bool ALIGN_EPI = false, bool SP2 = false>
; __device__ __forceinline__ void gemm_phase(PG8_LAS unsigned char* lds, const Gemm g, const Sched& S, const Epi& E) {
;     ...
;         if (!has_next) break;
;         if constexpr (!Epi::CHAIN) {
; #pragma unroll
;         for (int a = 0; a < 2; ++a)
; #pragma unroll
;             for (int b = 0; b < 2; ++b)
; #pragma unroll
;                 for (int m = 0; m < 4; ++m)
; #pragma unroll
;                     for (int n = 0; n < 2; ++n) acc[a][b][m][n] = (f32x4){0.f, 0.f, 0.f, 0.f};
;         }
;         cur = nxt; cA = nA; cB = nB; ++ui;
;         if constexpr (ALIGN_EPI) { if (wr == 1) PG8_BAR; }
;     }
;     ...
;     const unsigned long long tdrain_ = __builtin_amdgcn_s_memrealtime();
;     ...
;     PG8_WAIT_V(0);
;     if constexpr (!ALIGN_EPI) { if (wr == 0) PG8_BAR; }
;     PG8_BAR;
; __global__ void __launch_bounds__(NWAVES * 64, 2) mk_fwd(Args args) {
;     ...
;             if (cb >= 128) {
.LBB0_543:
	s_andn2_b64 vcc, exec, s[64:65]
	s_mov_b64 s[0:1], -1
	s_cbranch_vccnz .LBB0_391
	s_andn2_b64 vcc, exec, s[56:57]
	s_cbranch_vccnz .LBB0_390
	s_barrier
	s_branch .LBB0_390
.LBB0_548:
	s_waitcnt vmcnt(0)
	s_barrier
	s_cmpk_lt_i32 s21, 0x80
	s_cbranch_scc1 .LBB0_740
